# speedup vs baseline: 1.0071x; 1.0071x over previous
_Z11pwconv_mfmaPKfPK15HIP_vector_typeIjLj4EES0_Pf:
	s_load_dwordx4 s[12:15], s[0:1], 0x0
	s_load_dwordx4 s[16:19], s[0:1], 0x10
	s_and_b32 s20, s2, 7
	s_lshr_b32 s21, s2, 3
	s_lshr_b32 s37, s20, 1
	s_and_b32 s36, s20, 1
	s_mul_i32 s36, s36, 31
	s_add_i32 s36, s36, s21
	s_lshr_b32 s21, s36, 1
	s_and_b32 s36, s36, 1
	s_lshl_b32 s37, s37, 1
	s_add_i32 s20, s37, s36
	v_lshrrev_b32_e32 v1, 6, v0
	v_and_b32_e32 v2, 63, v0
	s_nop 0
	v_readfirstlane_b32 s22, v1
	s_nop 3
	s_lshl_b32 s23, s20, 3
	s_add_i32 s23, s23, s22
	s_mul_i32 s24, s23, 0x439200
	s_mul_i32 s25, s21, 0x1f0
	s_add_u32 s24, s24, s25
	s_lshl_b32 s25, s21, 17
	s_lshl_b32 s26, s22, 13
	s_add_u32 s25, s25, s26
	s_mul_i32 s27, s20, 0x1e080
	s_mul_i32 s36, s21, 0x1f0
	s_add_u32 s27, s27, s36
	v_min_u32_e32 v10, 61, v2
	v_lshlrev_b32_e32 v3, 3, v10
	v_lshlrev_b32_e32 v4, 4, v2
	v_cmp_lt_u32_e32 vcc, 30, v10
	s_nop 1
	v_cndmask_b32_e64 v5, 0, 1, vcc
	v_mul_u32_u24_e32 v6, 31, v5
	v_sub_u32_e32 v6, v10, v6
	v_lshl_add_u32 v7, v1, 1, v5
	v_and_b32_e32 v8, 7, v6
	v_xor_b32_e32 v7, v7, v8
	v_lshlrev_b32_e32 v7, 4, v7
	v_lshl_add_u32 v5, v6, 12, v7
	s_lshl_b32 s36, s22, 2
	s_add_i32 s36, s36, 0
	s_and_b32 s36, s36, 7
	s_lshl_b32 s37, s22, 14
	s_add_i32 s37, s37, 0x0
	v_xor_b32_e32 v6, s36, v2
	v_lshlrev_b32_e32 v6, 4, v6
	v_add_u32_e32 v6, s37, v6
	s_lshl_b32 s36, s22, 2
	s_add_i32 s36, s36, 1
	s_and_b32 s36, s36, 7
	s_lshl_b32 s37, s22, 14
	s_add_i32 s37, s37, 0x1000
	v_xor_b32_e32 v7, s36, v2
	v_lshlrev_b32_e32 v7, 4, v7
	v_add_u32_e32 v7, s37, v7
	s_lshl_b32 s36, s22, 2
	s_add_i32 s36, s36, 2
	s_and_b32 s36, s36, 7
	s_lshl_b32 s37, s22, 14
	s_add_i32 s37, s37, 0x2000
	v_xor_b32_e32 v8, s36, v2
	v_lshlrev_b32_e32 v8, 4, v8
	v_add_u32_e32 v8, s37, v8
	s_lshl_b32 s36, s22, 2
	s_add_i32 s36, s36, 3
	s_and_b32 s36, s36, 7
	s_lshl_b32 s37, s22, 14
	s_add_i32 s37, s37, 0x3000
	v_xor_b32_e32 v9, s36, v2
	v_lshlrev_b32_e32 v9, 4, v9
	v_add_u32_e32 v9, s37, v9
	s_lshl_b32 s36, s22, 11
	s_add_i32 s36, s36, 0x20000
	v_add_u32_e32 v254, s36, v4
	s_add_i32 s37, s22, 1
	s_min_u32 s37, s37, 7
	s_lshl_b32 s37, s37, 11
	s_add_i32 s37, s37, 0x20000
	v_add_u32_e32 v255, s37, v4
	v_lshrrev_b32_e32 v10, 5, v0
	v_lshrrev_b32_e32 v11, 1, v10
	v_mul_u32_u24_e32 v11, 0x3c10, v11
	v_and_b32_e32 v10, 1, v10
	v_mul_u32_u24_e32 v10, 0xf8, v10
	v_add_u32_e32 v11, v11, v10
	v_and_b32_e32 v10, 31, v0
	v_lshl_add_u32 v11, v10, 3, v11
	v_add_u32_e32 v11, s27, v11
	v_cmp_eq_u32_e32 vcc, 31, v10
	v_mov_b32_e32 v10, 0x7f000000
	s_nop 1
	v_cndmask_b32_e32 v11, v11, v10, vcc
	s_waitcnt lgkmcnt(0)
	s_add_u32 s4, s12, s24
	s_addc_u32 s5, s13, 0
	s_and_b32 s5, s5, 0xffff
	s_sub_u32 s6, 0x10e48000, s24
	s_mov_b32 s7, 0x20000
	s_add_u32 s8, s14, s25
	s_addc_u32 s9, s15, 0
	s_and_b32 s9, s9, 0xffff
	s_sub_u32 s10, 0x400000, s25
	s_mov_b32 s11, 0x20000
	s_mov_b32 s28, s16
	s_and_b32 s29, s17, 0xffff
	s_mov_b32 s30, 0xf0400
	s_mov_b32 s31, 0x20000
	s_mov_b32 s32, s18
	s_and_b32 s33, s19, 0xffff
	s_mov_b32 s34, 0xf04000
	s_mov_b32 s35, 0x20000
	s_cmp_ge_u32 s22, 4
	s_cbranch_scc0 .Lstag_done
	s_sleep 20
.Lstag_done:
	s_mov_b32 s40, 0x0
	s_mov_b32 s41, 0x21c90
	s_mov_b32 s42, 0x43920
	s_mov_b32 s43, 0x655b0
	s_mov_b32 s44, 0x87240
	s_mov_b32 s45, 0xa8ed0
	s_mov_b32 s46, 0xcab60
	s_mov_b32 s47, 0xec7f0
	buffer_load_dwordx2 v[44:45], v3, s[4:7], s40 offen nt
	buffer_load_dwordx2 v[46:47], v3, s[4:7], s41 offen nt
	buffer_load_dwordx2 v[48:49], v3, s[4:7], s42 offen nt
	buffer_load_dwordx2 v[50:51], v3, s[4:7], s43 offen nt
	buffer_load_dwordx2 v[52:53], v3, s[4:7], s44 offen nt
	buffer_load_dwordx2 v[54:55], v3, s[4:7], s45 offen nt
	buffer_load_dwordx2 v[56:57], v3, s[4:7], s46 offen nt
	buffer_load_dwordx2 v[58:59], v3, s[4:7], s47 offen nt
	s_mov_b32 s40, 0x10e480
	s_mov_b32 s41, 0x130110
	s_mov_b32 s42, 0x151da0
	s_mov_b32 s43, 0x173a30
	s_mov_b32 s44, 0x1956c0
	s_mov_b32 s45, 0x1b7350
	s_mov_b32 s46, 0x1d8fe0
	s_mov_b32 s47, 0x1fac70
	buffer_load_dwordx2 v[60:61], v3, s[4:7], s40 offen nt
	buffer_load_dwordx2 v[62:63], v3, s[4:7], s41 offen nt
	buffer_load_dwordx2 v[64:65], v3, s[4:7], s42 offen nt
	buffer_load_dwordx2 v[66:67], v3, s[4:7], s43 offen nt
	buffer_load_dwordx2 v[68:69], v3, s[4:7], s44 offen nt
	buffer_load_dwordx2 v[70:71], v3, s[4:7], s45 offen nt
	buffer_load_dwordx2 v[72:73], v3, s[4:7], s46 offen nt
	buffer_load_dwordx2 v[74:75], v3, s[4:7], s47 offen nt
	s_mov_b32 s40, 0x21c900
	s_mov_b32 s41, 0x23e590
	s_mov_b32 s42, 0x260220
	s_mov_b32 s43, 0x281eb0
	s_mov_b32 s44, 0x2a3b40
	s_mov_b32 s45, 0x2c57d0
	s_mov_b32 s46, 0x2e7460
	s_mov_b32 s47, 0x3090f0
	buffer_load_dwordx2 v[76:77], v3, s[4:7], s40 offen nt
	buffer_load_dwordx2 v[78:79], v3, s[4:7], s41 offen nt
	buffer_load_dwordx2 v[80:81], v3, s[4:7], s42 offen nt
	buffer_load_dwordx2 v[82:83], v3, s[4:7], s43 offen nt
	buffer_load_dwordx2 v[84:85], v3, s[4:7], s44 offen nt
	buffer_load_dwordx2 v[86:87], v3, s[4:7], s45 offen nt
	buffer_load_dwordx2 v[88:89], v3, s[4:7], s46 offen nt
	buffer_load_dwordx2 v[90:91], v3, s[4:7], s47 offen nt
	s_mov_b32 s40, 0x32ad80
	s_mov_b32 s41, 0x34ca10
	s_mov_b32 s42, 0x36e6a0
	s_mov_b32 s43, 0x390330
	s_mov_b32 s44, 0x3b1fc0
	s_mov_b32 s45, 0x3d3c50
	s_mov_b32 s46, 0x3f58e0
	s_mov_b32 s47, 0x417570
	buffer_load_dwordx2 v[92:93], v3, s[4:7], s40 offen nt
	buffer_load_dwordx2 v[94:95], v3, s[4:7], s41 offen nt
	buffer_load_dwordx2 v[96:97], v3, s[4:7], s42 offen nt
	buffer_load_dwordx2 v[98:99], v3, s[4:7], s43 offen nt
	buffer_load_dwordx2 v[100:101], v3, s[4:7], s44 offen nt
	buffer_load_dwordx2 v[102:103], v3, s[4:7], s45 offen nt
	buffer_load_dwordx2 v[104:105], v3, s[4:7], s46 offen nt
	buffer_load_dwordx2 v[106:107], v3, s[4:7], s47 offen nt
	buffer_load_dwordx2 v[252:253], v11, s[28:31], 0 offen
	s_mov_b32 s40, 0x0
	s_mov_b32 s41, 0x400
	s_mov_b32 s42, 0x800
	s_mov_b32 s43, 0xc00
	buffer_load_dwordx4 v[108:111], v4, s[8:11], s40 offen
	buffer_load_dwordx4 v[112:115], v4, s[8:11], s41 offen
	buffer_load_dwordx4 v[116:119], v4, s[8:11], s42 offen
	buffer_load_dwordx4 v[120:123], v4, s[8:11], s43 offen
	s_mov_b32 s40, 0x1000
	s_mov_b32 s41, 0x1400
	s_mov_b32 s42, 0x1800
	s_mov_b32 s43, 0x1c00
	buffer_load_dwordx4 v[124:127], v4, s[8:11], s40 offen
	buffer_load_dwordx4 v[128:131], v4, s[8:11], s41 offen
	buffer_load_dwordx4 v[132:135], v4, s[8:11], s42 offen
	buffer_load_dwordx4 v[136:139], v4, s[8:11], s43 offen
	s_mov_b32 s40, 0x10000
	s_mov_b32 s41, 0x10400
	s_mov_b32 s42, 0x10800
	s_mov_b32 s43, 0x10c00
	buffer_load_dwordx4 v[148:151], v4, s[8:11], s40 offen
	buffer_load_dwordx4 v[152:155], v4, s[8:11], s41 offen
	buffer_load_dwordx4 v[156:159], v4, s[8:11], s42 offen
	buffer_load_dwordx4 v[160:163], v4, s[8:11], s43 offen
	s_mov_b32 s40, 0x11000
	s_mov_b32 s41, 0x11400
	s_mov_b32 s42, 0x11800
	s_mov_b32 s43, 0x11c00
	buffer_load_dwordx4 v[164:167], v4, s[8:11], s40 offen
	buffer_load_dwordx4 v[168:171], v4, s[8:11], s41 offen
	buffer_load_dwordx4 v[172:175], v4, s[8:11], s42 offen
	buffer_load_dwordx4 v[176:179], v4, s[8:11], s43 offen
	s_waitcnt vmcnt(41)
	v_cvt_pkrtz_f16_f32 v12, v44, v46
	v_cvt_pkrtz_f16_f32 v13, v48, v50
	v_cvt_pkrtz_f16_f32 v14, v52, v54
	v_cvt_pkrtz_f16_f32 v15, v56, v58
	v_cvt_pkrtz_f16_f32 v16, v45, v47
	v_cvt_pkrtz_f16_f32 v17, v49, v51
	v_cvt_pkrtz_f16_f32 v18, v53, v55
	v_cvt_pkrtz_f16_f32 v19, v57, v59
	ds_write_b128 v5, v[12:15] offset:0
	ds_write_b128 v5, v[16:19] offset:2048
	s_waitcnt vmcnt(33)
	v_cvt_pkrtz_f16_f32 v12, v60, v62
	v_cvt_pkrtz_f16_f32 v13, v64, v66
	v_cvt_pkrtz_f16_f32 v14, v68, v70
	v_cvt_pkrtz_f16_f32 v15, v72, v74
	v_cvt_pkrtz_f16_f32 v16, v61, v63
	v_cvt_pkrtz_f16_f32 v17, v65, v67
	v_cvt_pkrtz_f16_f32 v18, v69, v71
	v_cvt_pkrtz_f16_f32 v19, v73, v75
	s_mov_b32 s40, 0x3c10
	s_mov_b32 s41, 0x258a0
	s_mov_b32 s42, 0x47530
	s_mov_b32 s43, 0x691c0
	s_mov_b32 s44, 0x8ae50
	s_mov_b32 s45, 0xacae0
	s_mov_b32 s46, 0xce770
	s_mov_b32 s47, 0xf0400
	buffer_load_dwordx2 v[44:45], v3, s[4:7], s40 offen nt
	buffer_load_dwordx2 v[46:47], v3, s[4:7], s41 offen nt
	buffer_load_dwordx2 v[48:49], v3, s[4:7], s42 offen nt
	buffer_load_dwordx2 v[50:51], v3, s[4:7], s43 offen nt
	buffer_load_dwordx2 v[52:53], v3, s[4:7], s44 offen nt
	buffer_load_dwordx2 v[54:55], v3, s[4:7], s45 offen nt
	buffer_load_dwordx2 v[56:57], v3, s[4:7], s46 offen nt
	buffer_load_dwordx2 v[58:59], v3, s[4:7], s47 offen nt
	ds_write_b128 v5, v[12:15] offset:256
	ds_write_b128 v5, v[16:19] offset:2304
	s_waitcnt vmcnt(33)
	v_cvt_pkrtz_f16_f32 v12, v76, v78
	v_cvt_pkrtz_f16_f32 v13, v80, v82
	v_cvt_pkrtz_f16_f32 v14, v84, v86
	v_cvt_pkrtz_f16_f32 v15, v88, v90
	v_cvt_pkrtz_f16_f32 v16, v77, v79
	v_cvt_pkrtz_f16_f32 v17, v81, v83
	v_cvt_pkrtz_f16_f32 v18, v85, v87
	v_cvt_pkrtz_f16_f32 v19, v89, v91
	s_mov_b32 s40, 0x112090
	s_mov_b32 s41, 0x133d20
	s_mov_b32 s42, 0x1559b0
	s_mov_b32 s43, 0x177640
	s_mov_b32 s44, 0x1992d0
	s_mov_b32 s45, 0x1baf60
	s_mov_b32 s46, 0x1dcbf0
	s_mov_b32 s47, 0x1fe880
	buffer_load_dwordx2 v[60:61], v3, s[4:7], s40 offen nt
	buffer_load_dwordx2 v[62:63], v3, s[4:7], s41 offen nt
	buffer_load_dwordx2 v[64:65], v3, s[4:7], s42 offen nt
	buffer_load_dwordx2 v[66:67], v3, s[4:7], s43 offen nt
	buffer_load_dwordx2 v[68:69], v3, s[4:7], s44 offen nt
	buffer_load_dwordx2 v[70:71], v3, s[4:7], s45 offen nt
	buffer_load_dwordx2 v[72:73], v3, s[4:7], s46 offen nt
	buffer_load_dwordx2 v[74:75], v3, s[4:7], s47 offen nt
	ds_write_b128 v5, v[12:15] offset:512
	ds_write_b128 v5, v[16:19] offset:2560
	s_waitcnt vmcnt(33)
	v_cvt_pkrtz_f16_f32 v12, v92, v94
	v_cvt_pkrtz_f16_f32 v13, v96, v98
	v_cvt_pkrtz_f16_f32 v14, v100, v102
	v_cvt_pkrtz_f16_f32 v15, v104, v106
	v_cvt_pkrtz_f16_f32 v16, v93, v95
	v_cvt_pkrtz_f16_f32 v17, v97, v99
	v_cvt_pkrtz_f16_f32 v18, v101, v103
	v_cvt_pkrtz_f16_f32 v19, v105, v107
	s_mov_b32 s40, 0x220510
	s_mov_b32 s41, 0x2421a0
	s_mov_b32 s42, 0x263e30
	s_mov_b32 s43, 0x285ac0
	s_mov_b32 s44, 0x2a7750
	s_mov_b32 s45, 0x2c93e0
	s_mov_b32 s46, 0x2eb070
	s_mov_b32 s47, 0x30cd00
	buffer_load_dwordx2 v[76:77], v3, s[4:7], s40 offen nt
	buffer_load_dwordx2 v[78:79], v3, s[4:7], s41 offen nt
	buffer_load_dwordx2 v[80:81], v3, s[4:7], s42 offen nt
	buffer_load_dwordx2 v[82:83], v3, s[4:7], s43 offen nt
	buffer_load_dwordx2 v[84:85], v3, s[4:7], s44 offen nt
	buffer_load_dwordx2 v[86:87], v3, s[4:7], s45 offen nt
	buffer_load_dwordx2 v[88:89], v3, s[4:7], s46 offen nt
	buffer_load_dwordx2 v[90:91], v3, s[4:7], s47 offen nt
	ds_write_b128 v5, v[12:15] offset:768
	ds_write_b128 v5, v[16:19] offset:2816
	s_waitcnt lgkmcnt(0)
	s_barrier
	s_waitcnt vmcnt(24)
	ds_write_b128 v254, v[108:111] offset:0
	ds_write_b128 v254, v[112:115] offset:1024
	ds_write_b128 v254, v[148:151] offset:16384
	ds_write_b128 v254, v[152:155] offset:17408
	s_waitcnt lgkmcnt(0)
	s_barrier
	ds_read_b128 v[140:143], v255 offset:0
	ds_read_b128 v[144:147], v255 offset:1024
	ds_read_b128 v[180:183], v255 offset:16384
	ds_read_b128 v[184:187], v255 offset:17408
	ds_read_b128 v[12:15], v6 offset:0
	ds_read_b128 v[16:19], v6 offset:2048
	ds_read_b128 v[20:23], v7 offset:0
	ds_read_b128 v[24:27], v7 offset:2048
	ds_read_b128 v[28:31], v8 offset:0
	ds_read_b128 v[32:35], v8 offset:2048
	ds_read_b128 v[36:39], v9 offset:0
	ds_read_b128 v[40:43], v9 offset:2048
	s_waitcnt lgkmcnt(7)
	v_mfma_f32_16x16x32_f16 v[188:191], v[108:111], v[12:15], 0
	v_mfma_f32_16x16x32_f16 v[220:223], v[148:151], v[12:15], 0
	s_waitcnt lgkmcnt(6)
	v_mfma_f32_16x16x32_f16 v[192:195], v[112:115], v[16:19], 0
	v_mfma_f32_16x16x32_f16 v[224:227], v[152:155], v[16:19], 0
	s_waitcnt lgkmcnt(5)
	v_mfma_f32_16x16x32_f16 v[196:199], v[116:119], v[20:23], 0
	v_mfma_f32_16x16x32_f16 v[228:231], v[156:159], v[20:23], 0
	s_waitcnt lgkmcnt(4)
	v_mfma_f32_16x16x32_f16 v[200:203], v[120:123], v[24:27], 0
	v_mfma_f32_16x16x32_f16 v[232:235], v[160:163], v[24:27], 0
	s_waitcnt lgkmcnt(3)
	v_mfma_f32_16x16x32_f16 v[204:207], v[124:127], v[28:31], 0
	v_mfma_f32_16x16x32_f16 v[236:239], v[164:167], v[28:31], 0
	s_waitcnt lgkmcnt(2)
	v_mfma_f32_16x16x32_f16 v[208:211], v[128:131], v[32:35], 0
	v_mfma_f32_16x16x32_f16 v[240:243], v[168:171], v[32:35], 0
	s_waitcnt lgkmcnt(1)
	v_mfma_f32_16x16x32_f16 v[212:215], v[132:135], v[36:39], 0
	v_mfma_f32_16x16x32_f16 v[244:247], v[172:175], v[36:39], 0
	s_waitcnt lgkmcnt(0)
	v_mfma_f32_16x16x32_f16 v[216:219], v[136:139], v[40:43], 0
	v_mfma_f32_16x16x32_f16 v[248:251], v[176:179], v[40:43], 0
	s_mov_b32 s40, 0x32e990
	s_mov_b32 s41, 0x350620
	s_mov_b32 s42, 0x3722b0
	s_mov_b32 s43, 0x393f40
	s_mov_b32 s44, 0x3b5bd0
	s_mov_b32 s45, 0x3d7860
	s_mov_b32 s46, 0x3f94f0
	s_mov_b32 s47, 0x41b180
	buffer_load_dwordx2 v[92:93], v3, s[4:7], s40 offen nt
	buffer_load_dwordx2 v[94:95], v3, s[4:7], s41 offen nt
	buffer_load_dwordx2 v[96:97], v3, s[4:7], s42 offen nt
	buffer_load_dwordx2 v[98:99], v3, s[4:7], s43 offen nt
	buffer_load_dwordx2 v[100:101], v3, s[4:7], s44 offen nt
	buffer_load_dwordx2 v[102:103], v3, s[4:7], s45 offen nt
	buffer_load_dwordx2 v[104:105], v3, s[4:7], s46 offen nt
	buffer_load_dwordx2 v[106:107], v3, s[4:7], s47 offen nt
	s_waitcnt vmcnt(24)
	v_cvt_pkrtz_f16_f32 v12, v44, v46
	v_cvt_pkrtz_f16_f32 v13, v48, v50
	v_cvt_pkrtz_f16_f32 v14, v52, v54
	v_cvt_pkrtz_f16_f32 v15, v56, v58
	v_cvt_pkrtz_f16_f32 v16, v45, v47
	v_cvt_pkrtz_f16_f32 v17, v49, v51
	v_cvt_pkrtz_f16_f32 v18, v53, v55
	v_cvt_pkrtz_f16_f32 v19, v57, v59
	ds_write_b128 v5, v[12:15] offset:1024
	ds_write_b128 v5, v[16:19] offset:3072
	s_waitcnt vmcnt(16)
	v_cvt_pkrtz_f16_f32 v12, v60, v62
	v_cvt_pkrtz_f16_f32 v13, v64, v66
	v_cvt_pkrtz_f16_f32 v14, v68, v70
	v_cvt_pkrtz_f16_f32 v15, v72, v74
	v_cvt_pkrtz_f16_f32 v16, v61, v63
	v_cvt_pkrtz_f16_f32 v17, v65, v67
	v_cvt_pkrtz_f16_f32 v18, v69, v71
	v_cvt_pkrtz_f16_f32 v19, v73, v75
	s_mov_b32 s40, 0x7820
	s_mov_b32 s41, 0x294b0
	s_mov_b32 s42, 0x4b140
	s_mov_b32 s43, 0x6cdd0
	s_mov_b32 s44, 0x8ea60
	s_mov_b32 s45, 0xb06f0
	s_mov_b32 s46, 0xd2380
	s_mov_b32 s47, 0xf4010
	buffer_load_dwordx2 v[44:45], v3, s[4:7], s40 offen nt
	buffer_load_dwordx2 v[46:47], v3, s[4:7], s41 offen nt
	buffer_load_dwordx2 v[48:49], v3, s[4:7], s42 offen nt
	buffer_load_dwordx2 v[50:51], v3, s[4:7], s43 offen nt
	buffer_load_dwordx2 v[52:53], v3, s[4:7], s44 offen nt
	buffer_load_dwordx2 v[54:55], v3, s[4:7], s45 offen nt
	buffer_load_dwordx2 v[56:57], v3, s[4:7], s46 offen nt
	buffer_load_dwordx2 v[58:59], v3, s[4:7], s47 offen nt
	ds_write_b128 v5, v[12:15] offset:1280
	ds_write_b128 v5, v[16:19] offset:3328
	s_waitcnt vmcnt(16)
	v_cvt_pkrtz_f16_f32 v12, v76, v78
	v_cvt_pkrtz_f16_f32 v13, v80, v82
	v_cvt_pkrtz_f16_f32 v14, v84, v86
	v_cvt_pkrtz_f16_f32 v15, v88, v90
	v_cvt_pkrtz_f16_f32 v16, v77, v79
	v_cvt_pkrtz_f16_f32 v17, v81, v83
	v_cvt_pkrtz_f16_f32 v18, v85, v87
	v_cvt_pkrtz_f16_f32 v19, v89, v91
	s_mov_b32 s40, 0x115ca0
	s_mov_b32 s41, 0x137930
	s_mov_b32 s42, 0x1595c0
	s_mov_b32 s43, 0x17b250
	s_mov_b32 s44, 0x19cee0
	s_mov_b32 s45, 0x1beb70
	s_mov_b32 s46, 0x1e0800
	s_mov_b32 s47, 0x202490
	buffer_load_dwordx2 v[60:61], v3, s[4:7], s40 offen nt
	buffer_load_dwordx2 v[62:63], v3, s[4:7], s41 offen nt
	buffer_load_dwordx2 v[64:65], v3, s[4:7], s42 offen nt
	buffer_load_dwordx2 v[66:67], v3, s[4:7], s43 offen nt
	buffer_load_dwordx2 v[68:69], v3, s[4:7], s44 offen nt
	buffer_load_dwordx2 v[70:71], v3, s[4:7], s45 offen nt
	buffer_load_dwordx2 v[72:73], v3, s[4:7], s46 offen nt
	buffer_load_dwordx2 v[74:75], v3, s[4:7], s47 offen nt
	ds_write_b128 v5, v[12:15] offset:1536
	ds_write_b128 v5, v[16:19] offset:3584
	s_waitcnt vmcnt(16)
	v_cvt_pkrtz_f16_f32 v12, v92, v94
	v_cvt_pkrtz_f16_f32 v13, v96, v98
	v_cvt_pkrtz_f16_f32 v14, v100, v102
	v_cvt_pkrtz_f16_f32 v15, v104, v106
	v_cvt_pkrtz_f16_f32 v16, v93, v95
	v_cvt_pkrtz_f16_f32 v17, v97, v99
	v_cvt_pkrtz_f16_f32 v18, v101, v103
	v_cvt_pkrtz_f16_f32 v19, v105, v107
	s_mov_b32 s40, 0x224120
	s_mov_b32 s41, 0x245db0
	s_mov_b32 s42, 0x267a40
	s_mov_b32 s43, 0x2896d0
	s_mov_b32 s44, 0x2ab360
	s_mov_b32 s45, 0x2ccff0
	s_mov_b32 s46, 0x2eec80
	s_mov_b32 s47, 0x310910
	buffer_load_dwordx2 v[76:77], v3, s[4:7], s40 offen nt
	buffer_load_dwordx2 v[78:79], v3, s[4:7], s41 offen nt
	buffer_load_dwordx2 v[80:81], v3, s[4:7], s42 offen nt
	buffer_load_dwordx2 v[82:83], v3, s[4:7], s43 offen nt
	buffer_load_dwordx2 v[84:85], v3, s[4:7], s44 offen nt
	buffer_load_dwordx2 v[86:87], v3, s[4:7], s45 offen nt
	buffer_load_dwordx2 v[88:89], v3, s[4:7], s46 offen nt
	buffer_load_dwordx2 v[90:91], v3, s[4:7], s47 offen nt
	ds_write_b128 v5, v[12:15] offset:1792
	ds_write_b128 v5, v[16:19] offset:3840
	s_waitcnt lgkmcnt(0)
	s_barrier
	ds_read_b128 v[12:15], v6 offset:1024
	ds_read_b128 v[16:19], v6 offset:3072
	ds_read_b128 v[20:23], v7 offset:1024
	ds_read_b128 v[24:27], v7 offset:3072
	ds_read_b128 v[28:31], v8 offset:1024
	ds_read_b128 v[32:35], v8 offset:3072
	ds_read_b128 v[36:39], v9 offset:1024
	ds_read_b128 v[40:43], v9 offset:3072
	s_waitcnt lgkmcnt(7)
	v_mfma_f32_16x16x32_f16 v[188:191], v[112:115], v[12:15], v[188:191]
	v_mfma_f32_16x16x32_f16 v[220:223], v[152:155], v[12:15], v[220:223]
	s_waitcnt lgkmcnt(6)
	v_mfma_f32_16x16x32_f16 v[192:195], v[116:119], v[16:19], v[192:195]
	v_mfma_f32_16x16x32_f16 v[224:227], v[156:159], v[16:19], v[224:227]
	s_waitcnt lgkmcnt(5)
	v_mfma_f32_16x16x32_f16 v[196:199], v[120:123], v[20:23], v[196:199]
	v_mfma_f32_16x16x32_f16 v[228:231], v[160:163], v[20:23], v[228:231]
	s_waitcnt lgkmcnt(4)
	v_mfma_f32_16x16x32_f16 v[200:203], v[124:127], v[24:27], v[200:203]
	v_mfma_f32_16x16x32_f16 v[232:235], v[164:167], v[24:27], v[232:235]
	s_waitcnt lgkmcnt(3)
	v_mfma_f32_16x16x32_f16 v[204:207], v[128:131], v[28:31], v[204:207]
	v_mfma_f32_16x16x32_f16 v[236:239], v[168:171], v[28:31], v[236:239]
	s_waitcnt lgkmcnt(2)
	v_mfma_f32_16x16x32_f16 v[208:211], v[132:135], v[32:35], v[208:211]
	v_mfma_f32_16x16x32_f16 v[240:243], v[172:175], v[32:35], v[240:243]
	s_waitcnt lgkmcnt(1)
	v_mfma_f32_16x16x32_f16 v[212:215], v[136:139], v[36:39], v[212:215]
	v_mfma_f32_16x16x32_f16 v[244:247], v[176:179], v[36:39], v[244:247]
	s_waitcnt lgkmcnt(0)
	v_mfma_f32_16x16x32_f16 v[216:219], v[140:143], v[40:43], v[216:219]
	v_mfma_f32_16x16x32_f16 v[248:251], v[180:183], v[40:43], v[248:251]
	s_mov_b32 s40, 0x3325a0
	s_mov_b32 s41, 0x354230
	s_mov_b32 s42, 0x375ec0
	s_mov_b32 s43, 0x397b50
	s_mov_b32 s44, 0x3b97e0
	s_mov_b32 s45, 0x3db470
	s_mov_b32 s46, 0x3fd100
	s_mov_b32 s47, 0x41ed90
	buffer_load_dwordx2 v[92:93], v3, s[4:7], s40 offen nt
	buffer_load_dwordx2 v[94:95], v3, s[4:7], s41 offen nt
	buffer_load_dwordx2 v[96:97], v3, s[4:7], s42 offen nt
	buffer_load_dwordx2 v[98:99], v3, s[4:7], s43 offen nt
	buffer_load_dwordx2 v[100:101], v3, s[4:7], s44 offen nt
	buffer_load_dwordx2 v[102:103], v3, s[4:7], s45 offen nt
	buffer_load_dwordx2 v[104:105], v3, s[4:7], s46 offen nt
	buffer_load_dwordx2 v[106:107], v3, s[4:7], s47 offen nt
	s_waitcnt vmcnt(24)
	v_cvt_pkrtz_f16_f32 v12, v44, v46
	v_cvt_pkrtz_f16_f32 v13, v48, v50
	v_cvt_pkrtz_f16_f32 v14, v52, v54
	v_cvt_pkrtz_f16_f32 v15, v56, v58
	v_cvt_pkrtz_f16_f32 v16, v45, v47
	v_cvt_pkrtz_f16_f32 v17, v49, v51
	v_cvt_pkrtz_f16_f32 v18, v53, v55
	v_cvt_pkrtz_f16_f32 v19, v57, v59
	ds_write_b128 v5, v[12:15] offset:0
	ds_write_b128 v5, v[16:19] offset:2048
	s_waitcnt vmcnt(16)
	v_cvt_pkrtz_f16_f32 v12, v60, v62
	v_cvt_pkrtz_f16_f32 v13, v64, v66
	v_cvt_pkrtz_f16_f32 v14, v68, v70
	v_cvt_pkrtz_f16_f32 v15, v72, v74
	v_cvt_pkrtz_f16_f32 v16, v61, v63
	v_cvt_pkrtz_f16_f32 v17, v65, v67
	v_cvt_pkrtz_f16_f32 v18, v69, v71
	v_cvt_pkrtz_f16_f32 v19, v73, v75
	s_mov_b32 s40, 0xb430
	s_mov_b32 s41, 0x2d0c0
	s_mov_b32 s42, 0x4ed50
	s_mov_b32 s43, 0x709e0
	s_mov_b32 s44, 0x92670
	s_mov_b32 s45, 0xb4300
	s_mov_b32 s46, 0xd5f90
	s_mov_b32 s47, 0xf7c20
	buffer_load_dwordx2 v[44:45], v3, s[4:7], s40 offen nt
	buffer_load_dwordx2 v[46:47], v3, s[4:7], s41 offen nt
	buffer_load_dwordx2 v[48:49], v3, s[4:7], s42 offen nt
	buffer_load_dwordx2 v[50:51], v3, s[4:7], s43 offen nt
	buffer_load_dwordx2 v[52:53], v3, s[4:7], s44 offen nt
	buffer_load_dwordx2 v[54:55], v3, s[4:7], s45 offen nt
	buffer_load_dwordx2 v[56:57], v3, s[4:7], s46 offen nt
	buffer_load_dwordx2 v[58:59], v3, s[4:7], s47 offen nt
	ds_write_b128 v5, v[12:15] offset:256
	ds_write_b128 v5, v[16:19] offset:2304
	s_waitcnt vmcnt(16)
	v_cvt_pkrtz_f16_f32 v12, v76, v78
	v_cvt_pkrtz_f16_f32 v13, v80, v82
	v_cvt_pkrtz_f16_f32 v14, v84, v86
	v_cvt_pkrtz_f16_f32 v15, v88, v90
	v_cvt_pkrtz_f16_f32 v16, v77, v79
	v_cvt_pkrtz_f16_f32 v17, v81, v83
	v_cvt_pkrtz_f16_f32 v18, v85, v87
	v_cvt_pkrtz_f16_f32 v19, v89, v91
	s_mov_b32 s40, 0x1198b0
	s_mov_b32 s41, 0x13b540
	s_mov_b32 s42, 0x15d1d0
	s_mov_b32 s43, 0x17ee60
	s_mov_b32 s44, 0x1a0af0
	s_mov_b32 s45, 0x1c2780
	s_mov_b32 s46, 0x1e4410
	s_mov_b32 s47, 0x2060a0
	buffer_load_dwordx2 v[60:61], v3, s[4:7], s40 offen nt
	buffer_load_dwordx2 v[62:63], v3, s[4:7], s41 offen nt
	buffer_load_dwordx2 v[64:65], v3, s[4:7], s42 offen nt
	buffer_load_dwordx2 v[66:67], v3, s[4:7], s43 offen nt
	buffer_load_dwordx2 v[68:69], v3, s[4:7], s44 offen nt
	buffer_load_dwordx2 v[70:71], v3, s[4:7], s45 offen nt
	buffer_load_dwordx2 v[72:73], v3, s[4:7], s46 offen nt
	buffer_load_dwordx2 v[74:75], v3, s[4:7], s47 offen nt
	ds_write_b128 v5, v[12:15] offset:512
	ds_write_b128 v5, v[16:19] offset:2560
	s_waitcnt vmcnt(16)
	v_cvt_pkrtz_f16_f32 v12, v92, v94
	v_cvt_pkrtz_f16_f32 v13, v96, v98
	v_cvt_pkrtz_f16_f32 v14, v100, v102
	v_cvt_pkrtz_f16_f32 v15, v104, v106
	v_cvt_pkrtz_f16_f32 v16, v93, v95
	v_cvt_pkrtz_f16_f32 v17, v97, v99
	v_cvt_pkrtz_f16_f32 v18, v101, v103
	v_cvt_pkrtz_f16_f32 v19, v105, v107
	s_mov_b32 s40, 0x227d30
	s_mov_b32 s41, 0x2499c0
	s_mov_b32 s42, 0x26b650
	s_mov_b32 s43, 0x28d2e0
	s_mov_b32 s44, 0x2aef70
	s_mov_b32 s45, 0x2d0c00
	s_mov_b32 s46, 0x2f2890
	s_mov_b32 s47, 0x314520
	buffer_load_dwordx2 v[76:77], v3, s[4:7], s40 offen nt
	buffer_load_dwordx2 v[78:79], v3, s[4:7], s41 offen nt
	buffer_load_dwordx2 v[80:81], v3, s[4:7], s42 offen nt
	buffer_load_dwordx2 v[82:83], v3, s[4:7], s43 offen nt
	buffer_load_dwordx2 v[84:85], v3, s[4:7], s44 offen nt
	buffer_load_dwordx2 v[86:87], v3, s[4:7], s45 offen nt
	buffer_load_dwordx2 v[88:89], v3, s[4:7], s46 offen nt
	buffer_load_dwordx2 v[90:91], v3, s[4:7], s47 offen nt
	ds_write_b128 v5, v[12:15] offset:768
	ds_write_b128 v5, v[16:19] offset:2816
	s_waitcnt lgkmcnt(0)
	s_barrier
	ds_read_b128 v[12:15], v6 offset:0
	ds_read_b128 v[16:19], v6 offset:2048
	ds_read_b128 v[20:23], v7 offset:0
	ds_read_b128 v[24:27], v7 offset:2048
	ds_read_b128 v[28:31], v8 offset:0
	ds_read_b128 v[32:35], v8 offset:2048
	ds_read_b128 v[36:39], v9 offset:0
	ds_read_b128 v[40:43], v9 offset:2048
	s_waitcnt lgkmcnt(7)
	v_mfma_f32_16x16x32_f16 v[188:191], v[116:119], v[12:15], v[188:191]
	v_mfma_f32_16x16x32_f16 v[220:223], v[156:159], v[12:15], v[220:223]
	s_waitcnt lgkmcnt(6)
	v_mfma_f32_16x16x32_f16 v[192:195], v[120:123], v[16:19], v[192:195]
	v_mfma_f32_16x16x32_f16 v[224:227], v[160:163], v[16:19], v[224:227]
	s_waitcnt lgkmcnt(5)
	v_mfma_f32_16x16x32_f16 v[196:199], v[124:127], v[20:23], v[196:199]
	v_mfma_f32_16x16x32_f16 v[228:231], v[164:167], v[20:23], v[228:231]
	s_waitcnt lgkmcnt(4)
	v_mfma_f32_16x16x32_f16 v[200:203], v[128:131], v[24:27], v[200:203]
	v_mfma_f32_16x16x32_f16 v[232:235], v[168:171], v[24:27], v[232:235]
	s_waitcnt lgkmcnt(3)
	v_mfma_f32_16x16x32_f16 v[204:207], v[132:135], v[28:31], v[204:207]
	v_mfma_f32_16x16x32_f16 v[236:239], v[172:175], v[28:31], v[236:239]
	s_waitcnt lgkmcnt(2)
	v_mfma_f32_16x16x32_f16 v[208:211], v[136:139], v[32:35], v[208:211]
	v_mfma_f32_16x16x32_f16 v[240:243], v[176:179], v[32:35], v[240:243]
	s_waitcnt lgkmcnt(1)
	v_mfma_f32_16x16x32_f16 v[212:215], v[140:143], v[36:39], v[212:215]
	v_mfma_f32_16x16x32_f16 v[244:247], v[180:183], v[36:39], v[244:247]
	s_waitcnt lgkmcnt(0)
	v_mfma_f32_16x16x32_f16 v[216:219], v[144:147], v[40:43], v[216:219]
	v_mfma_f32_16x16x32_f16 v[248:251], v[184:187], v[40:43], v[248:251]
	s_mov_b32 s40, 0x20000
	s_mov_b32 s41, 0x20400
	s_mov_b32 s42, 0x20800
	s_mov_b32 s43, 0x20c00
	buffer_load_dwordx4 v[108:111], v4, s[8:11], s40 offen
	buffer_load_dwordx4 v[112:115], v4, s[8:11], s41 offen
	buffer_load_dwordx4 v[116:119], v4, s[8:11], s42 offen
	buffer_load_dwordx4 v[120:123], v4, s[8:11], s43 offen
	s_mov_b32 s40, 0x21000
	s_mov_b32 s41, 0x21400
	s_mov_b32 s42, 0x21800
	s_mov_b32 s43, 0x21c00
	buffer_load_dwordx4 v[124:127], v4, s[8:11], s40 offen
	buffer_load_dwordx4 v[128:131], v4, s[8:11], s41 offen
	buffer_load_dwordx4 v[132:135], v4, s[8:11], s42 offen
	buffer_load_dwordx4 v[136:139], v4, s[8:11], s43 offen
	s_mov_b32 s40, 0x3361b0
	s_mov_b32 s41, 0x357e40
	s_mov_b32 s42, 0x379ad0
	s_mov_b32 s43, 0x39b760
	s_mov_b32 s44, 0x3bd3f0
	s_mov_b32 s45, 0x3df080
	s_mov_b32 s46, 0x400d10
	s_mov_b32 s47, 0x4229a0
	buffer_load_dwordx2 v[92:93], v3, s[4:7], s40 offen nt
	buffer_load_dwordx2 v[94:95], v3, s[4:7], s41 offen nt
	buffer_load_dwordx2 v[96:97], v3, s[4:7], s42 offen nt
	buffer_load_dwordx2 v[98:99], v3, s[4:7], s43 offen nt
	buffer_load_dwordx2 v[100:101], v3, s[4:7], s44 offen nt
	buffer_load_dwordx2 v[102:103], v3, s[4:7], s45 offen nt
	buffer_load_dwordx2 v[104:105], v3, s[4:7], s46 offen nt
	buffer_load_dwordx2 v[106:107], v3, s[4:7], s47 offen nt
	s_waitcnt vmcnt(32)
	v_cvt_pkrtz_f16_f32 v12, v44, v46
	v_cvt_pkrtz_f16_f32 v13, v48, v50
	v_cvt_pkrtz_f16_f32 v14, v52, v54
	v_cvt_pkrtz_f16_f32 v15, v56, v58
	v_cvt_pkrtz_f16_f32 v16, v45, v47
	v_cvt_pkrtz_f16_f32 v17, v49, v51
	v_cvt_pkrtz_f16_f32 v18, v53, v55
	v_cvt_pkrtz_f16_f32 v19, v57, v59
	ds_write_b128 v5, v[12:15] offset:1024
	ds_write_b128 v5, v[16:19] offset:3072
	s_waitcnt vmcnt(24)
	v_cvt_pkrtz_f16_f32 v12, v60, v62
	v_cvt_pkrtz_f16_f32 v13, v64, v66
	v_cvt_pkrtz_f16_f32 v14, v68, v70
	v_cvt_pkrtz_f16_f32 v15, v72, v74
	v_cvt_pkrtz_f16_f32 v16, v61, v63
	v_cvt_pkrtz_f16_f32 v17, v65, v67
	v_cvt_pkrtz_f16_f32 v18, v69, v71
	v_cvt_pkrtz_f16_f32 v19, v73, v75
	s_mov_b32 s40, 0xf040
	s_mov_b32 s41, 0x30cd0
	s_mov_b32 s42, 0x52960
	s_mov_b32 s43, 0x745f0
	s_mov_b32 s44, 0x96280
	s_mov_b32 s45, 0xb7f10
	s_mov_b32 s46, 0xd9ba0
	s_mov_b32 s47, 0xfb830
	buffer_load_dwordx2 v[44:45], v3, s[4:7], s40 offen nt
	buffer_load_dwordx2 v[46:47], v3, s[4:7], s41 offen nt
	buffer_load_dwordx2 v[48:49], v3, s[4:7], s42 offen nt
	buffer_load_dwordx2 v[50:51], v3, s[4:7], s43 offen nt
	buffer_load_dwordx2 v[52:53], v3, s[4:7], s44 offen nt
	buffer_load_dwordx2 v[54:55], v3, s[4:7], s45 offen nt
	buffer_load_dwordx2 v[56:57], v3, s[4:7], s46 offen nt
	buffer_load_dwordx2 v[58:59], v3, s[4:7], s47 offen nt
	ds_write_b128 v5, v[12:15] offset:1280
	ds_write_b128 v5, v[16:19] offset:3328
	s_waitcnt vmcnt(24)
	v_cvt_pkrtz_f16_f32 v12, v76, v78
	v_cvt_pkrtz_f16_f32 v13, v80, v82
	v_cvt_pkrtz_f16_f32 v14, v84, v86
	v_cvt_pkrtz_f16_f32 v15, v88, v90
	v_cvt_pkrtz_f16_f32 v16, v77, v79
	v_cvt_pkrtz_f16_f32 v17, v81, v83
	v_cvt_pkrtz_f16_f32 v18, v85, v87
	v_cvt_pkrtz_f16_f32 v19, v89, v91
	s_mov_b32 s40, 0x11d4c0
	s_mov_b32 s41, 0x13f150
	s_mov_b32 s42, 0x160de0
	s_mov_b32 s43, 0x182a70
	s_mov_b32 s44, 0x1a4700
	s_mov_b32 s45, 0x1c6390
	s_mov_b32 s46, 0x1e8020
	s_mov_b32 s47, 0x209cb0
	buffer_load_dwordx2 v[60:61], v3, s[4:7], s40 offen nt
	buffer_load_dwordx2 v[62:63], v3, s[4:7], s41 offen nt
	buffer_load_dwordx2 v[64:65], v3, s[4:7], s42 offen nt
	buffer_load_dwordx2 v[66:67], v3, s[4:7], s43 offen nt
	buffer_load_dwordx2 v[68:69], v3, s[4:7], s44 offen nt
	buffer_load_dwordx2 v[70:71], v3, s[4:7], s45 offen nt
	buffer_load_dwordx2 v[72:73], v3, s[4:7], s46 offen nt
	buffer_load_dwordx2 v[74:75], v3, s[4:7], s47 offen nt
	ds_write_b128 v5, v[12:15] offset:1536
	ds_write_b128 v5, v[16:19] offset:3584
	s_waitcnt vmcnt(16)
	v_cvt_pkrtz_f16_f32 v12, v92, v94
	v_cvt_pkrtz_f16_f32 v13, v96, v98
	v_cvt_pkrtz_f16_f32 v14, v100, v102
	v_cvt_pkrtz_f16_f32 v15, v104, v106
	v_cvt_pkrtz_f16_f32 v16, v93, v95
	v_cvt_pkrtz_f16_f32 v17, v97, v99
	v_cvt_pkrtz_f16_f32 v18, v101, v103
	v_cvt_pkrtz_f16_f32 v19, v105, v107
	s_mov_b32 s40, 0x22b940
	s_mov_b32 s41, 0x24d5d0
	s_mov_b32 s42, 0x26f260
	s_mov_b32 s43, 0x290ef0
	s_mov_b32 s44, 0x2b2b80
	s_mov_b32 s45, 0x2d4810
	s_mov_b32 s46, 0x2f64a0
	s_mov_b32 s47, 0x318130
	buffer_load_dwordx2 v[76:77], v3, s[4:7], s40 offen nt
	buffer_load_dwordx2 v[78:79], v3, s[4:7], s41 offen nt
	buffer_load_dwordx2 v[80:81], v3, s[4:7], s42 offen nt
	buffer_load_dwordx2 v[82:83], v3, s[4:7], s43 offen nt
	buffer_load_dwordx2 v[84:85], v3, s[4:7], s44 offen nt
	buffer_load_dwordx2 v[86:87], v3, s[4:7], s45 offen nt
	buffer_load_dwordx2 v[88:89], v3, s[4:7], s46 offen nt
	buffer_load_dwordx2 v[90:91], v3, s[4:7], s47 offen nt
	ds_write_b128 v5, v[12:15] offset:1792
	ds_write_b128 v5, v[16:19] offset:3840
	s_waitcnt lgkmcnt(0)
	s_barrier
	ds_write_b128 v254, v[108:111] offset:0
	ds_write_b128 v254, v[112:115] offset:1024
	s_waitcnt lgkmcnt(0)
	s_barrier
	ds_read_b128 v[140:143], v255 offset:0
	ds_read_b128 v[144:147], v255 offset:1024
	ds_read_b128 v[12:15], v6 offset:1024
	ds_read_b128 v[16:19], v6 offset:3072
	ds_read_b128 v[20:23], v7 offset:1024
	ds_read_b128 v[24:27], v7 offset:3072
	ds_read_b128 v[28:31], v8 offset:1024
	ds_read_b128 v[32:35], v8 offset:3072
	ds_read_b128 v[36:39], v9 offset:1024
	ds_read_b128 v[40:43], v9 offset:3072
	s_waitcnt lgkmcnt(7)
	v_mfma_f32_16x16x32_f16 v[188:191], v[148:151], v[12:15], v[188:191]
	v_mfma_f32_16x16x32_f16 v[220:223], v[108:111], v[12:15], v[220:223]
	s_waitcnt lgkmcnt(6)
	v_mfma_f32_16x16x32_f16 v[192:195], v[152:155], v[16:19], v[192:195]
	v_mfma_f32_16x16x32_f16 v[224:227], v[112:115], v[16:19], v[224:227]
	s_waitcnt lgkmcnt(5)
	v_mfma_f32_16x16x32_f16 v[196:199], v[156:159], v[20:23], v[196:199]
	v_mfma_f32_16x16x32_f16 v[228:231], v[116:119], v[20:23], v[228:231]
	s_waitcnt lgkmcnt(4)
	v_mfma_f32_16x16x32_f16 v[200:203], v[160:163], v[24:27], v[200:203]
	v_mfma_f32_16x16x32_f16 v[232:235], v[120:123], v[24:27], v[232:235]
	s_waitcnt lgkmcnt(3)
	v_mfma_f32_16x16x32_f16 v[204:207], v[164:167], v[28:31], v[204:207]
	v_mfma_f32_16x16x32_f16 v[236:239], v[124:127], v[28:31], v[236:239]
	s_waitcnt lgkmcnt(2)
	v_mfma_f32_16x16x32_f16 v[208:211], v[168:171], v[32:35], v[208:211]
	v_mfma_f32_16x16x32_f16 v[240:243], v[128:131], v[32:35], v[240:243]
	s_waitcnt lgkmcnt(1)
	v_mfma_f32_16x16x32_f16 v[212:215], v[172:175], v[36:39], v[212:215]
	v_mfma_f32_16x16x32_f16 v[244:247], v[132:135], v[36:39], v[244:247]
	s_waitcnt lgkmcnt(0)
	v_mfma_f32_16x16x32_f16 v[216:219], v[176:179], v[40:43], v[216:219]
	v_mfma_f32_16x16x32_f16 v[248:251], v[136:139], v[40:43], v[248:251]
	s_mov_b32 s40, 0x339dc0
	s_mov_b32 s41, 0x35ba50
	s_mov_b32 s42, 0x37d6e0
	s_mov_b32 s43, 0x39f370
	s_mov_b32 s44, 0x3c1000
	s_mov_b32 s45, 0x3e2c90
	s_mov_b32 s46, 0x404920
	s_mov_b32 s47, 0x4265b0
	buffer_load_dwordx2 v[92:93], v3, s[4:7], s40 offen nt
	buffer_load_dwordx2 v[94:95], v3, s[4:7], s41 offen nt
	buffer_load_dwordx2 v[96:97], v3, s[4:7], s42 offen nt
	buffer_load_dwordx2 v[98:99], v3, s[4:7], s43 offen nt
	buffer_load_dwordx2 v[100:101], v3, s[4:7], s44 offen nt
	buffer_load_dwordx2 v[102:103], v3, s[4:7], s45 offen nt
	buffer_load_dwordx2 v[104:105], v3, s[4:7], s46 offen nt
	buffer_load_dwordx2 v[106:107], v3, s[4:7], s47 offen nt
	s_waitcnt vmcnt(24)
	v_cvt_pkrtz_f16_f32 v12, v44, v46
	v_cvt_pkrtz_f16_f32 v13, v48, v50
	v_cvt_pkrtz_f16_f32 v14, v52, v54
	v_cvt_pkrtz_f16_f32 v15, v56, v58
	v_cvt_pkrtz_f16_f32 v16, v45, v47
	v_cvt_pkrtz_f16_f32 v17, v49, v51
	v_cvt_pkrtz_f16_f32 v18, v53, v55
	v_cvt_pkrtz_f16_f32 v19, v57, v59
	ds_write_b128 v5, v[12:15] offset:0
	ds_write_b128 v5, v[16:19] offset:2048
	s_waitcnt vmcnt(16)
	v_cvt_pkrtz_f16_f32 v12, v60, v62
	v_cvt_pkrtz_f16_f32 v13, v64, v66
	v_cvt_pkrtz_f16_f32 v14, v68, v70
	v_cvt_pkrtz_f16_f32 v15, v72, v74
	v_cvt_pkrtz_f16_f32 v16, v61, v63
	v_cvt_pkrtz_f16_f32 v17, v65, v67
	v_cvt_pkrtz_f16_f32 v18, v69, v71
	v_cvt_pkrtz_f16_f32 v19, v73, v75
	s_mov_b32 s40, 0x12c50
	s_mov_b32 s41, 0x348e0
	s_mov_b32 s42, 0x56570
	s_mov_b32 s43, 0x78200
	s_mov_b32 s44, 0x99e90
	s_mov_b32 s45, 0xbbb20
	s_mov_b32 s46, 0xdd7b0
	s_mov_b32 s47, 0xff440
	buffer_load_dwordx2 v[44:45], v3, s[4:7], s40 offen nt
	buffer_load_dwordx2 v[46:47], v3, s[4:7], s41 offen nt
	buffer_load_dwordx2 v[48:49], v3, s[4:7], s42 offen nt
	buffer_load_dwordx2 v[50:51], v3, s[4:7], s43 offen nt
	buffer_load_dwordx2 v[52:53], v3, s[4:7], s44 offen nt
	buffer_load_dwordx2 v[54:55], v3, s[4:7], s45 offen nt
	buffer_load_dwordx2 v[56:57], v3, s[4:7], s46 offen nt
	buffer_load_dwordx2 v[58:59], v3, s[4:7], s47 offen nt
	ds_write_b128 v5, v[12:15] offset:256
	ds_write_b128 v5, v[16:19] offset:2304
	s_waitcnt vmcnt(16)
	v_cvt_pkrtz_f16_f32 v12, v76, v78
	v_cvt_pkrtz_f16_f32 v13, v80, v82
	v_cvt_pkrtz_f16_f32 v14, v84, v86
	v_cvt_pkrtz_f16_f32 v15, v88, v90
	v_cvt_pkrtz_f16_f32 v16, v77, v79
	v_cvt_pkrtz_f16_f32 v17, v81, v83
	v_cvt_pkrtz_f16_f32 v18, v85, v87
	v_cvt_pkrtz_f16_f32 v19, v89, v91
	s_mov_b32 s40, 0x1210d0
	s_mov_b32 s41, 0x142d60
	s_mov_b32 s42, 0x1649f0
	s_mov_b32 s43, 0x186680
	s_mov_b32 s44, 0x1a8310
	s_mov_b32 s45, 0x1c9fa0
	s_mov_b32 s46, 0x1ebc30
	s_mov_b32 s47, 0x20d8c0
	buffer_load_dwordx2 v[60:61], v3, s[4:7], s40 offen nt
	buffer_load_dwordx2 v[62:63], v3, s[4:7], s41 offen nt
	buffer_load_dwordx2 v[64:65], v3, s[4:7], s42 offen nt
	buffer_load_dwordx2 v[66:67], v3, s[4:7], s43 offen nt
	buffer_load_dwordx2 v[68:69], v3, s[4:7], s44 offen nt
	buffer_load_dwordx2 v[70:71], v3, s[4:7], s45 offen nt
	buffer_load_dwordx2 v[72:73], v3, s[4:7], s46 offen nt
	buffer_load_dwordx2 v[74:75], v3, s[4:7], s47 offen nt
	ds_write_b128 v5, v[12:15] offset:512
	ds_write_b128 v5, v[16:19] offset:2560
	s_waitcnt vmcnt(16)
	v_cvt_pkrtz_f16_f32 v12, v92, v94
	v_cvt_pkrtz_f16_f32 v13, v96, v98
	v_cvt_pkrtz_f16_f32 v14, v100, v102
	v_cvt_pkrtz_f16_f32 v15, v104, v106
	v_cvt_pkrtz_f16_f32 v16, v93, v95
	v_cvt_pkrtz_f16_f32 v17, v97, v99
	v_cvt_pkrtz_f16_f32 v18, v101, v103
	v_cvt_pkrtz_f16_f32 v19, v105, v107
	s_mov_b32 s40, 0x22f550
	s_mov_b32 s41, 0x2511e0
	s_mov_b32 s42, 0x272e70
	s_mov_b32 s43, 0x294b00
	s_mov_b32 s44, 0x2b6790
	s_mov_b32 s45, 0x2d8420
	s_mov_b32 s46, 0x2fa0b0
	s_mov_b32 s47, 0x31bd40
	buffer_load_dwordx2 v[76:77], v3, s[4:7], s40 offen nt
	buffer_load_dwordx2 v[78:79], v3, s[4:7], s41 offen nt
	buffer_load_dwordx2 v[80:81], v3, s[4:7], s42 offen nt
	buffer_load_dwordx2 v[82:83], v3, s[4:7], s43 offen nt
	buffer_load_dwordx2 v[84:85], v3, s[4:7], s44 offen nt
	buffer_load_dwordx2 v[86:87], v3, s[4:7], s45 offen nt
	buffer_load_dwordx2 v[88:89], v3, s[4:7], s46 offen nt
	buffer_load_dwordx2 v[90:91], v3, s[4:7], s47 offen nt
	ds_write_b128 v5, v[12:15] offset:768
	ds_write_b128 v5, v[16:19] offset:2816
	s_waitcnt lgkmcnt(0)
	s_barrier
	ds_read_b128 v[12:15], v6 offset:0
	ds_read_b128 v[16:19], v6 offset:2048
	ds_read_b128 v[20:23], v7 offset:0
	ds_read_b128 v[24:27], v7 offset:2048
	ds_read_b128 v[28:31], v8 offset:0
	ds_read_b128 v[32:35], v8 offset:2048
	ds_read_b128 v[36:39], v9 offset:0
	ds_read_b128 v[40:43], v9 offset:2048
	s_waitcnt lgkmcnt(7)
	v_mfma_f32_16x16x32_f16 v[188:191], v[152:155], v[12:15], v[188:191]
	v_mfma_f32_16x16x32_f16 v[220:223], v[112:115], v[12:15], v[220:223]
	s_waitcnt lgkmcnt(6)
	v_mfma_f32_16x16x32_f16 v[192:195], v[156:159], v[16:19], v[192:195]
	v_mfma_f32_16x16x32_f16 v[224:227], v[116:119], v[16:19], v[224:227]
	s_waitcnt lgkmcnt(5)
	v_mfma_f32_16x16x32_f16 v[196:199], v[160:163], v[20:23], v[196:199]
	v_mfma_f32_16x16x32_f16 v[228:231], v[120:123], v[20:23], v[228:231]
	s_waitcnt lgkmcnt(4)
	v_mfma_f32_16x16x32_f16 v[200:203], v[164:167], v[24:27], v[200:203]
	v_mfma_f32_16x16x32_f16 v[232:235], v[124:127], v[24:27], v[232:235]
	s_waitcnt lgkmcnt(3)
	v_mfma_f32_16x16x32_f16 v[204:207], v[168:171], v[28:31], v[204:207]
	v_mfma_f32_16x16x32_f16 v[236:239], v[128:131], v[28:31], v[236:239]
	s_waitcnt lgkmcnt(2)
	v_mfma_f32_16x16x32_f16 v[208:211], v[172:175], v[32:35], v[208:211]
	v_mfma_f32_16x16x32_f16 v[240:243], v[132:135], v[32:35], v[240:243]
	s_waitcnt lgkmcnt(1)
	v_mfma_f32_16x16x32_f16 v[212:215], v[176:179], v[36:39], v[212:215]
	v_mfma_f32_16x16x32_f16 v[244:247], v[136:139], v[36:39], v[244:247]
	s_waitcnt lgkmcnt(0)
	v_mfma_f32_16x16x32_f16 v[216:219], v[180:183], v[40:43], v[216:219]
	v_mfma_f32_16x16x32_f16 v[248:251], v[140:143], v[40:43], v[248:251]
	s_mov_b32 s40, 0x33d9d0
	s_mov_b32 s41, 0x35f660
	s_mov_b32 s42, 0x3812f0
	s_mov_b32 s43, 0x3a2f80
	s_mov_b32 s44, 0x3c4c10
	s_mov_b32 s45, 0x3e68a0
	s_mov_b32 s46, 0x408530
	s_mov_b32 s47, 0x42a1c0
	buffer_load_dwordx2 v[92:93], v3, s[4:7], s40 offen nt
	buffer_load_dwordx2 v[94:95], v3, s[4:7], s41 offen nt
	buffer_load_dwordx2 v[96:97], v3, s[4:7], s42 offen nt
	buffer_load_dwordx2 v[98:99], v3, s[4:7], s43 offen nt
	buffer_load_dwordx2 v[100:101], v3, s[4:7], s44 offen nt
	buffer_load_dwordx2 v[102:103], v3, s[4:7], s45 offen nt
	buffer_load_dwordx2 v[104:105], v3, s[4:7], s46 offen nt
	buffer_load_dwordx2 v[106:107], v3, s[4:7], s47 offen nt
	s_waitcnt vmcnt(24)
	v_cvt_pkrtz_f16_f32 v12, v44, v46
	v_cvt_pkrtz_f16_f32 v13, v48, v50
	v_cvt_pkrtz_f16_f32 v14, v52, v54
	v_cvt_pkrtz_f16_f32 v15, v56, v58
	v_cvt_pkrtz_f16_f32 v16, v45, v47
	v_cvt_pkrtz_f16_f32 v17, v49, v51
	v_cvt_pkrtz_f16_f32 v18, v53, v55
	v_cvt_pkrtz_f16_f32 v19, v57, v59
	ds_write_b128 v5, v[12:15] offset:1024
	ds_write_b128 v5, v[16:19] offset:3072
	s_waitcnt vmcnt(16)
	v_cvt_pkrtz_f16_f32 v12, v60, v62
	v_cvt_pkrtz_f16_f32 v13, v64, v66
	v_cvt_pkrtz_f16_f32 v14, v68, v70
	v_cvt_pkrtz_f16_f32 v15, v72, v74
	v_cvt_pkrtz_f16_f32 v16, v61, v63
	v_cvt_pkrtz_f16_f32 v17, v65, v67
	v_cvt_pkrtz_f16_f32 v18, v69, v71
	v_cvt_pkrtz_f16_f32 v19, v73, v75
	s_mov_b32 s40, 0x16860
	s_mov_b32 s41, 0x384f0
	s_mov_b32 s42, 0x5a180
	s_mov_b32 s43, 0x7be10
	s_mov_b32 s44, 0x9daa0
	s_mov_b32 s45, 0xbf730
	s_mov_b32 s46, 0xe13c0
	s_mov_b32 s47, 0x103050
	buffer_load_dwordx2 v[44:45], v3, s[4:7], s40 offen nt
	buffer_load_dwordx2 v[46:47], v3, s[4:7], s41 offen nt
	buffer_load_dwordx2 v[48:49], v3, s[4:7], s42 offen nt
	buffer_load_dwordx2 v[50:51], v3, s[4:7], s43 offen nt
	buffer_load_dwordx2 v[52:53], v3, s[4:7], s44 offen nt
	buffer_load_dwordx2 v[54:55], v3, s[4:7], s45 offen nt
	buffer_load_dwordx2 v[56:57], v3, s[4:7], s46 offen nt
	buffer_load_dwordx2 v[58:59], v3, s[4:7], s47 offen nt
	ds_write_b128 v5, v[12:15] offset:1280
	ds_write_b128 v5, v[16:19] offset:3328
	s_waitcnt vmcnt(16)
	v_cvt_pkrtz_f16_f32 v12, v76, v78
	v_cvt_pkrtz_f16_f32 v13, v80, v82
	v_cvt_pkrtz_f16_f32 v14, v84, v86
	v_cvt_pkrtz_f16_f32 v15, v88, v90
	v_cvt_pkrtz_f16_f32 v16, v77, v79
	v_cvt_pkrtz_f16_f32 v17, v81, v83
	v_cvt_pkrtz_f16_f32 v18, v85, v87
	v_cvt_pkrtz_f16_f32 v19, v89, v91
	s_mov_b32 s40, 0x124ce0
	s_mov_b32 s41, 0x146970
	s_mov_b32 s42, 0x168600
	s_mov_b32 s43, 0x18a290
	s_mov_b32 s44, 0x1abf20
	s_mov_b32 s45, 0x1cdbb0
	s_mov_b32 s46, 0x1ef840
	s_mov_b32 s47, 0x2114d0
	buffer_load_dwordx2 v[60:61], v3, s[4:7], s40 offen nt
	buffer_load_dwordx2 v[62:63], v3, s[4:7], s41 offen nt
	buffer_load_dwordx2 v[64:65], v3, s[4:7], s42 offen nt
	buffer_load_dwordx2 v[66:67], v3, s[4:7], s43 offen nt
	buffer_load_dwordx2 v[68:69], v3, s[4:7], s44 offen nt
	buffer_load_dwordx2 v[70:71], v3, s[4:7], s45 offen nt
	buffer_load_dwordx2 v[72:73], v3, s[4:7], s46 offen nt
	buffer_load_dwordx2 v[74:75], v3, s[4:7], s47 offen nt
	ds_write_b128 v5, v[12:15] offset:1536
	ds_write_b128 v5, v[16:19] offset:3584
	s_waitcnt vmcnt(16)
	v_cvt_pkrtz_f16_f32 v12, v92, v94
	v_cvt_pkrtz_f16_f32 v13, v96, v98
	v_cvt_pkrtz_f16_f32 v14, v100, v102
	v_cvt_pkrtz_f16_f32 v15, v104, v106
	v_cvt_pkrtz_f16_f32 v16, v93, v95
	v_cvt_pkrtz_f16_f32 v17, v97, v99
	v_cvt_pkrtz_f16_f32 v18, v101, v103
	v_cvt_pkrtz_f16_f32 v19, v105, v107
	s_mov_b32 s40, 0x233160
	s_mov_b32 s41, 0x254df0
	s_mov_b32 s42, 0x276a80
	s_mov_b32 s43, 0x298710
	s_mov_b32 s44, 0x2ba3a0
	s_mov_b32 s45, 0x2dc030
	s_mov_b32 s46, 0x2fdcc0
	s_mov_b32 s47, 0x31f950
	buffer_load_dwordx2 v[76:77], v3, s[4:7], s40 offen nt
	buffer_load_dwordx2 v[78:79], v3, s[4:7], s41 offen nt
	buffer_load_dwordx2 v[80:81], v3, s[4:7], s42 offen nt
	buffer_load_dwordx2 v[82:83], v3, s[4:7], s43 offen nt
	buffer_load_dwordx2 v[84:85], v3, s[4:7], s44 offen nt
	buffer_load_dwordx2 v[86:87], v3, s[4:7], s45 offen nt
	buffer_load_dwordx2 v[88:89], v3, s[4:7], s46 offen nt
	buffer_load_dwordx2 v[90:91], v3, s[4:7], s47 offen nt
	ds_write_b128 v5, v[12:15] offset:1792
	ds_write_b128 v5, v[16:19] offset:3840
	s_waitcnt lgkmcnt(0)
	s_barrier
	ds_read_b128 v[12:15], v6 offset:1024
	ds_read_b128 v[16:19], v6 offset:3072
	ds_read_b128 v[20:23], v7 offset:1024
	ds_read_b128 v[24:27], v7 offset:3072
	ds_read_b128 v[28:31], v8 offset:1024
	ds_read_b128 v[32:35], v8 offset:3072
	ds_read_b128 v[36:39], v9 offset:1024
	ds_read_b128 v[40:43], v9 offset:3072
	s_waitcnt lgkmcnt(7)
	v_mfma_f32_16x16x32_f16 v[188:191], v[156:159], v[12:15], v[188:191]
	v_mfma_f32_16x16x32_f16 v[220:223], v[116:119], v[12:15], v[220:223]
	s_waitcnt lgkmcnt(6)
	v_mfma_f32_16x16x32_f16 v[192:195], v[160:163], v[16:19], v[192:195]
	v_mfma_f32_16x16x32_f16 v[224:227], v[120:123], v[16:19], v[224:227]
	s_waitcnt lgkmcnt(5)
	v_mfma_f32_16x16x32_f16 v[196:199], v[164:167], v[20:23], v[196:199]
	v_mfma_f32_16x16x32_f16 v[228:231], v[124:127], v[20:23], v[228:231]
	s_waitcnt lgkmcnt(4)
	v_mfma_f32_16x16x32_f16 v[200:203], v[168:171], v[24:27], v[200:203]
	v_mfma_f32_16x16x32_f16 v[232:235], v[128:131], v[24:27], v[232:235]
	s_waitcnt lgkmcnt(3)
	v_mfma_f32_16x16x32_f16 v[204:207], v[172:175], v[28:31], v[204:207]
	v_mfma_f32_16x16x32_f16 v[236:239], v[132:135], v[28:31], v[236:239]
	s_waitcnt lgkmcnt(2)
	v_mfma_f32_16x16x32_f16 v[208:211], v[176:179], v[32:35], v[208:211]
	v_mfma_f32_16x16x32_f16 v[240:243], v[136:139], v[32:35], v[240:243]
	s_waitcnt lgkmcnt(1)
	v_mfma_f32_16x16x32_f16 v[212:215], v[180:183], v[36:39], v[212:215]
	v_mfma_f32_16x16x32_f16 v[244:247], v[140:143], v[36:39], v[244:247]
	s_waitcnt lgkmcnt(0)
	v_mfma_f32_16x16x32_f16 v[216:219], v[184:187], v[40:43], v[216:219]
	v_mfma_f32_16x16x32_f16 v[248:251], v[144:147], v[40:43], v[248:251]
	s_mov_b32 s40, 0x30000
	s_mov_b32 s41, 0x30400
	s_mov_b32 s42, 0x30800
	s_mov_b32 s43, 0x30c00
	buffer_load_dwordx4 v[148:151], v4, s[8:11], s40 offen
	buffer_load_dwordx4 v[152:155], v4, s[8:11], s41 offen
	buffer_load_dwordx4 v[156:159], v4, s[8:11], s42 offen
	buffer_load_dwordx4 v[160:163], v4, s[8:11], s43 offen
	s_mov_b32 s40, 0x31000
	s_mov_b32 s41, 0x31400
	s_mov_b32 s42, 0x31800
	s_mov_b32 s43, 0x31c00
	buffer_load_dwordx4 v[164:167], v4, s[8:11], s40 offen
	buffer_load_dwordx4 v[168:171], v4, s[8:11], s41 offen
	buffer_load_dwordx4 v[172:175], v4, s[8:11], s42 offen
	buffer_load_dwordx4 v[176:179], v4, s[8:11], s43 offen
	s_mov_b32 s40, 0x3415e0
	s_mov_b32 s41, 0x363270
	s_mov_b32 s42, 0x384f00
	s_mov_b32 s43, 0x3a6b90
	s_mov_b32 s44, 0x3c8820
	s_mov_b32 s45, 0x3ea4b0
	s_mov_b32 s46, 0x40c140
	s_mov_b32 s47, 0x42ddd0
	buffer_load_dwordx2 v[92:93], v3, s[4:7], s40 offen nt
	buffer_load_dwordx2 v[94:95], v3, s[4:7], s41 offen nt
	buffer_load_dwordx2 v[96:97], v3, s[4:7], s42 offen nt
	buffer_load_dwordx2 v[98:99], v3, s[4:7], s43 offen nt
	buffer_load_dwordx2 v[100:101], v3, s[4:7], s44 offen nt
	buffer_load_dwordx2 v[102:103], v3, s[4:7], s45 offen nt
	buffer_load_dwordx2 v[104:105], v3, s[4:7], s46 offen nt
	buffer_load_dwordx2 v[106:107], v3, s[4:7], s47 offen nt
	s_waitcnt vmcnt(32)
	v_cvt_pkrtz_f16_f32 v12, v44, v46
	v_cvt_pkrtz_f16_f32 v13, v48, v50
	v_cvt_pkrtz_f16_f32 v14, v52, v54
	v_cvt_pkrtz_f16_f32 v15, v56, v58
	v_cvt_pkrtz_f16_f32 v16, v45, v47
	v_cvt_pkrtz_f16_f32 v17, v49, v51
	v_cvt_pkrtz_f16_f32 v18, v53, v55
	v_cvt_pkrtz_f16_f32 v19, v57, v59
	ds_write_b128 v5, v[12:15] offset:0
	ds_write_b128 v5, v[16:19] offset:2048
	s_waitcnt vmcnt(24)
	v_cvt_pkrtz_f16_f32 v12, v60, v62
	v_cvt_pkrtz_f16_f32 v13, v64, v66
	v_cvt_pkrtz_f16_f32 v14, v68, v70
	v_cvt_pkrtz_f16_f32 v15, v72, v74
	v_cvt_pkrtz_f16_f32 v16, v61, v63
	v_cvt_pkrtz_f16_f32 v17, v65, v67
	v_cvt_pkrtz_f16_f32 v18, v69, v71
	v_cvt_pkrtz_f16_f32 v19, v73, v75
	s_mov_b32 s40, 0x1a470
	s_mov_b32 s41, 0x3c100
	s_mov_b32 s42, 0x5dd90
	s_mov_b32 s43, 0x7fa20
	s_mov_b32 s44, 0xa16b0
	s_mov_b32 s45, 0xc3340
	s_mov_b32 s46, 0xe4fd0
	s_mov_b32 s47, 0x106c60
	buffer_load_dwordx2 v[44:45], v3, s[4:7], s40 offen nt
	buffer_load_dwordx2 v[46:47], v3, s[4:7], s41 offen nt
	buffer_load_dwordx2 v[48:49], v3, s[4:7], s42 offen nt
	buffer_load_dwordx2 v[50:51], v3, s[4:7], s43 offen nt
	buffer_load_dwordx2 v[52:53], v3, s[4:7], s44 offen nt
	buffer_load_dwordx2 v[54:55], v3, s[4:7], s45 offen nt
	buffer_load_dwordx2 v[56:57], v3, s[4:7], s46 offen nt
	buffer_load_dwordx2 v[58:59], v3, s[4:7], s47 offen nt
	ds_write_b128 v5, v[12:15] offset:256
	ds_write_b128 v5, v[16:19] offset:2304
	s_waitcnt vmcnt(24)
	v_cvt_pkrtz_f16_f32 v12, v76, v78
	v_cvt_pkrtz_f16_f32 v13, v80, v82
	v_cvt_pkrtz_f16_f32 v14, v84, v86
	v_cvt_pkrtz_f16_f32 v15, v88, v90
	v_cvt_pkrtz_f16_f32 v16, v77, v79
	v_cvt_pkrtz_f16_f32 v17, v81, v83
	v_cvt_pkrtz_f16_f32 v18, v85, v87
	v_cvt_pkrtz_f16_f32 v19, v89, v91
	s_mov_b32 s40, 0x1288f0
	s_mov_b32 s41, 0x14a580
	s_mov_b32 s42, 0x16c210
	s_mov_b32 s43, 0x18dea0
	s_mov_b32 s44, 0x1afb30
	s_mov_b32 s45, 0x1d17c0
	s_mov_b32 s46, 0x1f3450
	s_mov_b32 s47, 0x2150e0
	buffer_load_dwordx2 v[60:61], v3, s[4:7], s40 offen nt
	buffer_load_dwordx2 v[62:63], v3, s[4:7], s41 offen nt
	buffer_load_dwordx2 v[64:65], v3, s[4:7], s42 offen nt
	buffer_load_dwordx2 v[66:67], v3, s[4:7], s43 offen nt
	buffer_load_dwordx2 v[68:69], v3, s[4:7], s44 offen nt
	buffer_load_dwordx2 v[70:71], v3, s[4:7], s45 offen nt
	buffer_load_dwordx2 v[72:73], v3, s[4:7], s46 offen nt
	buffer_load_dwordx2 v[74:75], v3, s[4:7], s47 offen nt
	ds_write_b128 v5, v[12:15] offset:512
	ds_write_b128 v5, v[16:19] offset:2560
	s_waitcnt vmcnt(16)
	v_cvt_pkrtz_f16_f32 v12, v92, v94
	v_cvt_pkrtz_f16_f32 v13, v96, v98
	v_cvt_pkrtz_f16_f32 v14, v100, v102
	v_cvt_pkrtz_f16_f32 v15, v104, v106
	v_cvt_pkrtz_f16_f32 v16, v93, v95
	v_cvt_pkrtz_f16_f32 v17, v97, v99
	v_cvt_pkrtz_f16_f32 v18, v101, v103
	v_cvt_pkrtz_f16_f32 v19, v105, v107
	s_mov_b32 s40, 0x236d70
	s_mov_b32 s41, 0x258a00
	s_mov_b32 s42, 0x27a690
	s_mov_b32 s43, 0x29c320
	s_mov_b32 s44, 0x2bdfb0
	s_mov_b32 s45, 0x2dfc40
	s_mov_b32 s46, 0x3018d0
	s_mov_b32 s47, 0x323560
	buffer_load_dwordx2 v[76:77], v3, s[4:7], s40 offen nt
	buffer_load_dwordx2 v[78:79], v3, s[4:7], s41 offen nt
	buffer_load_dwordx2 v[80:81], v3, s[4:7], s42 offen nt
	buffer_load_dwordx2 v[82:83], v3, s[4:7], s43 offen nt
	buffer_load_dwordx2 v[84:85], v3, s[4:7], s44 offen nt
	buffer_load_dwordx2 v[86:87], v3, s[4:7], s45 offen nt
	buffer_load_dwordx2 v[88:89], v3, s[4:7], s46 offen nt
	buffer_load_dwordx2 v[90:91], v3, s[4:7], s47 offen nt
	ds_write_b128 v5, v[12:15] offset:768
	ds_write_b128 v5, v[16:19] offset:2816
	s_waitcnt lgkmcnt(0)
	s_barrier
	ds_write_b128 v254, v[148:151] offset:16384
	ds_write_b128 v254, v[152:155] offset:17408
	s_waitcnt lgkmcnt(0)
	s_barrier
	ds_read_b128 v[180:183], v255 offset:16384
	ds_read_b128 v[184:187], v255 offset:17408
	ds_read_b128 v[12:15], v6 offset:0
	ds_read_b128 v[16:19], v6 offset:2048
	ds_read_b128 v[20:23], v7 offset:0
	ds_read_b128 v[24:27], v7 offset:2048
	ds_read_b128 v[28:31], v8 offset:0
	ds_read_b128 v[32:35], v8 offset:2048
	ds_read_b128 v[36:39], v9 offset:0
	ds_read_b128 v[40:43], v9 offset:2048
	s_waitcnt lgkmcnt(7)
	v_mfma_f32_16x16x32_f16 v[188:191], v[108:111], v[12:15], v[188:191]
	v_mfma_f32_16x16x32_f16 v[220:223], v[148:151], v[12:15], v[220:223]
	s_waitcnt lgkmcnt(6)
	v_mfma_f32_16x16x32_f16 v[192:195], v[112:115], v[16:19], v[192:195]
	v_mfma_f32_16x16x32_f16 v[224:227], v[152:155], v[16:19], v[224:227]
	s_waitcnt lgkmcnt(5)
	v_mfma_f32_16x16x32_f16 v[196:199], v[116:119], v[20:23], v[196:199]
	v_mfma_f32_16x16x32_f16 v[228:231], v[156:159], v[20:23], v[228:231]
	s_waitcnt lgkmcnt(4)
	v_mfma_f32_16x16x32_f16 v[200:203], v[120:123], v[24:27], v[200:203]
	v_mfma_f32_16x16x32_f16 v[232:235], v[160:163], v[24:27], v[232:235]
	s_waitcnt lgkmcnt(3)
	v_mfma_f32_16x16x32_f16 v[204:207], v[124:127], v[28:31], v[204:207]
	v_mfma_f32_16x16x32_f16 v[236:239], v[164:167], v[28:31], v[236:239]
	s_waitcnt lgkmcnt(2)
	v_mfma_f32_16x16x32_f16 v[208:211], v[128:131], v[32:35], v[208:211]
	v_mfma_f32_16x16x32_f16 v[240:243], v[168:171], v[32:35], v[240:243]
	s_waitcnt lgkmcnt(1)
	v_mfma_f32_16x16x32_f16 v[212:215], v[132:135], v[36:39], v[212:215]
	v_mfma_f32_16x16x32_f16 v[244:247], v[172:175], v[36:39], v[244:247]
	s_waitcnt lgkmcnt(0)
	v_mfma_f32_16x16x32_f16 v[216:219], v[136:139], v[40:43], v[216:219]
	v_mfma_f32_16x16x32_f16 v[248:251], v[176:179], v[40:43], v[248:251]
	s_mov_b32 s40, 0x3451f0
	s_mov_b32 s41, 0x366e80
	s_mov_b32 s42, 0x388b10
	s_mov_b32 s43, 0x3aa7a0
	s_mov_b32 s44, 0x3cc430
	s_mov_b32 s45, 0x3ee0c0
	s_mov_b32 s46, 0x40fd50
	s_mov_b32 s47, 0x4319e0
	buffer_load_dwordx2 v[92:93], v3, s[4:7], s40 offen nt
	buffer_load_dwordx2 v[94:95], v3, s[4:7], s41 offen nt
	buffer_load_dwordx2 v[96:97], v3, s[4:7], s42 offen nt
	buffer_load_dwordx2 v[98:99], v3, s[4:7], s43 offen nt
	buffer_load_dwordx2 v[100:101], v3, s[4:7], s44 offen nt
	buffer_load_dwordx2 v[102:103], v3, s[4:7], s45 offen nt
	buffer_load_dwordx2 v[104:105], v3, s[4:7], s46 offen nt
	buffer_load_dwordx2 v[106:107], v3, s[4:7], s47 offen nt
	s_waitcnt vmcnt(24)
	v_cvt_pkrtz_f16_f32 v12, v44, v46
	v_cvt_pkrtz_f16_f32 v13, v48, v50
	v_cvt_pkrtz_f16_f32 v14, v52, v54
	v_cvt_pkrtz_f16_f32 v15, v56, v58
	v_cvt_pkrtz_f16_f32 v16, v45, v47
	v_cvt_pkrtz_f16_f32 v17, v49, v51
	v_cvt_pkrtz_f16_f32 v18, v53, v55
	v_cvt_pkrtz_f16_f32 v19, v57, v59
	ds_write_b128 v5, v[12:15] offset:1024
	ds_write_b128 v5, v[16:19] offset:3072
	s_waitcnt vmcnt(16)
	v_cvt_pkrtz_f16_f32 v12, v60, v62
	v_cvt_pkrtz_f16_f32 v13, v64, v66
	v_cvt_pkrtz_f16_f32 v14, v68, v70
	v_cvt_pkrtz_f16_f32 v15, v72, v74
	v_cvt_pkrtz_f16_f32 v16, v61, v63
	v_cvt_pkrtz_f16_f32 v17, v65, v67
	v_cvt_pkrtz_f16_f32 v18, v69, v71
	v_cvt_pkrtz_f16_f32 v19, v73, v75
	s_mov_b32 s40, 0x1e080
	s_mov_b32 s41, 0x3fd10
	s_mov_b32 s42, 0x619a0
	s_mov_b32 s43, 0x83630
	s_mov_b32 s44, 0xa52c0
	s_mov_b32 s45, 0xc6f50
	s_mov_b32 s46, 0xe8be0
	s_mov_b32 s47, 0x10a870
	buffer_load_dwordx2 v[44:45], v3, s[4:7], s40 offen nt
	buffer_load_dwordx2 v[46:47], v3, s[4:7], s41 offen nt
	buffer_load_dwordx2 v[48:49], v3, s[4:7], s42 offen nt
	buffer_load_dwordx2 v[50:51], v3, s[4:7], s43 offen nt
	buffer_load_dwordx2 v[52:53], v3, s[4:7], s44 offen nt
	buffer_load_dwordx2 v[54:55], v3, s[4:7], s45 offen nt
	buffer_load_dwordx2 v[56:57], v3, s[4:7], s46 offen nt
	buffer_load_dwordx2 v[58:59], v3, s[4:7], s47 offen nt
	ds_write_b128 v5, v[12:15] offset:1280
	ds_write_b128 v5, v[16:19] offset:3328
	s_waitcnt vmcnt(16)
	v_cvt_pkrtz_f16_f32 v12, v76, v78
	v_cvt_pkrtz_f16_f32 v13, v80, v82
	v_cvt_pkrtz_f16_f32 v14, v84, v86
	v_cvt_pkrtz_f16_f32 v15, v88, v90
	v_cvt_pkrtz_f16_f32 v16, v77, v79
	v_cvt_pkrtz_f16_f32 v17, v81, v83
	v_cvt_pkrtz_f16_f32 v18, v85, v87
	v_cvt_pkrtz_f16_f32 v19, v89, v91
	s_mov_b32 s40, 0x12c500
	s_mov_b32 s41, 0x14e190
	s_mov_b32 s42, 0x16fe20
	s_mov_b32 s43, 0x191ab0
	s_mov_b32 s44, 0x1b3740
	s_mov_b32 s45, 0x1d53d0
	s_mov_b32 s46, 0x1f7060
	s_mov_b32 s47, 0x218cf0
	buffer_load_dwordx2 v[60:61], v3, s[4:7], s40 offen nt
	buffer_load_dwordx2 v[62:63], v3, s[4:7], s41 offen nt
	buffer_load_dwordx2 v[64:65], v3, s[4:7], s42 offen nt
	buffer_load_dwordx2 v[66:67], v3, s[4:7], s43 offen nt
	buffer_load_dwordx2 v[68:69], v3, s[4:7], s44 offen nt
	buffer_load_dwordx2 v[70:71], v3, s[4:7], s45 offen nt
	buffer_load_dwordx2 v[72:73], v3, s[4:7], s46 offen nt
	buffer_load_dwordx2 v[74:75], v3, s[4:7], s47 offen nt
	ds_write_b128 v5, v[12:15] offset:1536
	ds_write_b128 v5, v[16:19] offset:3584
	s_waitcnt vmcnt(16)
	v_cvt_pkrtz_f16_f32 v12, v92, v94
	v_cvt_pkrtz_f16_f32 v13, v96, v98
	v_cvt_pkrtz_f16_f32 v14, v100, v102
	v_cvt_pkrtz_f16_f32 v15, v104, v106
	v_cvt_pkrtz_f16_f32 v16, v93, v95
	v_cvt_pkrtz_f16_f32 v17, v97, v99
	v_cvt_pkrtz_f16_f32 v18, v101, v103
	v_cvt_pkrtz_f16_f32 v19, v105, v107
	s_mov_b32 s40, 0x23a980
	s_mov_b32 s41, 0x25c610
	s_mov_b32 s42, 0x27e2a0
	s_mov_b32 s43, 0x29ff30
	s_mov_b32 s44, 0x2c1bc0
	s_mov_b32 s45, 0x2e3850
	s_mov_b32 s46, 0x3054e0
	s_mov_b32 s47, 0x327170
	buffer_load_dwordx2 v[76:77], v3, s[4:7], s40 offen nt
	buffer_load_dwordx2 v[78:79], v3, s[4:7], s41 offen nt
	buffer_load_dwordx2 v[80:81], v3, s[4:7], s42 offen nt
	buffer_load_dwordx2 v[82:83], v3, s[4:7], s43 offen nt
	buffer_load_dwordx2 v[84:85], v3, s[4:7], s44 offen nt
	buffer_load_dwordx2 v[86:87], v3, s[4:7], s45 offen nt
	buffer_load_dwordx2 v[88:89], v3, s[4:7], s46 offen nt
	buffer_load_dwordx2 v[90:91], v3, s[4:7], s47 offen nt
	ds_write_b128 v5, v[12:15] offset:1792
	ds_write_b128 v5, v[16:19] offset:3840
	s_waitcnt lgkmcnt(0)
	s_barrier
	ds_read_b128 v[12:15], v6 offset:1024
	ds_read_b128 v[16:19], v6 offset:3072
	ds_read_b128 v[20:23], v7 offset:1024
	ds_read_b128 v[24:27], v7 offset:3072
	ds_read_b128 v[28:31], v8 offset:1024
	ds_read_b128 v[32:35], v8 offset:3072
	ds_read_b128 v[36:39], v9 offset:1024
	ds_read_b128 v[40:43], v9 offset:3072
	s_waitcnt lgkmcnt(7)
	v_mfma_f32_16x16x32_f16 v[188:191], v[112:115], v[12:15], v[188:191]
	v_mfma_f32_16x16x32_f16 v[220:223], v[152:155], v[12:15], v[220:223]
	s_waitcnt lgkmcnt(6)
	v_mfma_f32_16x16x32_f16 v[192:195], v[116:119], v[16:19], v[192:195]
	v_mfma_f32_16x16x32_f16 v[224:227], v[156:159], v[16:19], v[224:227]
	s_waitcnt lgkmcnt(5)
	v_mfma_f32_16x16x32_f16 v[196:199], v[120:123], v[20:23], v[196:199]
	v_mfma_f32_16x16x32_f16 v[228:231], v[160:163], v[20:23], v[228:231]
	s_waitcnt lgkmcnt(4)
	v_mfma_f32_16x16x32_f16 v[200:203], v[124:127], v[24:27], v[200:203]
	v_mfma_f32_16x16x32_f16 v[232:235], v[164:167], v[24:27], v[232:235]
	s_waitcnt lgkmcnt(3)
	v_mfma_f32_16x16x32_f16 v[204:207], v[128:131], v[28:31], v[204:207]
	v_mfma_f32_16x16x32_f16 v[236:239], v[168:171], v[28:31], v[236:239]
	s_waitcnt lgkmcnt(2)
	v_mfma_f32_16x16x32_f16 v[208:211], v[132:135], v[32:35], v[208:211]
	v_mfma_f32_16x16x32_f16 v[240:243], v[172:175], v[32:35], v[240:243]
	s_waitcnt lgkmcnt(1)
	v_mfma_f32_16x16x32_f16 v[212:215], v[136:139], v[36:39], v[212:215]
	v_mfma_f32_16x16x32_f16 v[244:247], v[176:179], v[36:39], v[244:247]
	s_waitcnt lgkmcnt(0)
	v_mfma_f32_16x16x32_f16 v[216:219], v[140:143], v[40:43], v[216:219]
	v_mfma_f32_16x16x32_f16 v[248:251], v[180:183], v[40:43], v[248:251]
	s_mov_b32 s40, 0x348e00
	s_mov_b32 s41, 0x36aa90
	s_mov_b32 s42, 0x38c720
	s_mov_b32 s43, 0x3ae3b0
	s_mov_b32 s44, 0x3d0040
	s_mov_b32 s45, 0x3f1cd0
	s_mov_b32 s46, 0x413960
	s_mov_b32 s47, 0x4355f0
	buffer_load_dwordx2 v[92:93], v3, s[4:7], s40 offen nt
	buffer_load_dwordx2 v[94:95], v3, s[4:7], s41 offen nt
	buffer_load_dwordx2 v[96:97], v3, s[4:7], s42 offen nt
	buffer_load_dwordx2 v[98:99], v3, s[4:7], s43 offen nt
	buffer_load_dwordx2 v[100:101], v3, s[4:7], s44 offen nt
	buffer_load_dwordx2 v[102:103], v3, s[4:7], s45 offen nt
	buffer_load_dwordx2 v[104:105], v3, s[4:7], s46 offen nt
	buffer_load_dwordx2 v[106:107], v3, s[4:7], s47 offen nt
	s_waitcnt vmcnt(24)
	v_cvt_pkrtz_f16_f32 v12, v44, v46
	v_cvt_pkrtz_f16_f32 v13, v48, v50
	v_cvt_pkrtz_f16_f32 v14, v52, v54
	v_cvt_pkrtz_f16_f32 v15, v56, v58
	v_cvt_pkrtz_f16_f32 v16, v45, v47
	v_cvt_pkrtz_f16_f32 v17, v49, v51
	v_cvt_pkrtz_f16_f32 v18, v53, v55
	v_cvt_pkrtz_f16_f32 v19, v57, v59
	ds_write_b128 v5, v[12:15] offset:0
	ds_write_b128 v5, v[16:19] offset:2048
	s_waitcnt vmcnt(16)
	v_cvt_pkrtz_f16_f32 v12, v60, v62
	v_cvt_pkrtz_f16_f32 v13, v64, v66
	v_cvt_pkrtz_f16_f32 v14, v68, v70
	v_cvt_pkrtz_f16_f32 v15, v72, v74
	v_cvt_pkrtz_f16_f32 v16, v61, v63
	v_cvt_pkrtz_f16_f32 v17, v65, v67
	v_cvt_pkrtz_f16_f32 v18, v69, v71
	v_cvt_pkrtz_f16_f32 v19, v73, v75
	ds_write_b128 v5, v[12:15] offset:256
	ds_write_b128 v5, v[16:19] offset:2304
	s_waitcnt vmcnt(8)
	v_cvt_pkrtz_f16_f32 v12, v76, v78
	v_cvt_pkrtz_f16_f32 v13, v80, v82
	v_cvt_pkrtz_f16_f32 v14, v84, v86
	v_cvt_pkrtz_f16_f32 v15, v88, v90
	v_cvt_pkrtz_f16_f32 v16, v77, v79
	v_cvt_pkrtz_f16_f32 v17, v81, v83
	v_cvt_pkrtz_f16_f32 v18, v85, v87
	v_cvt_pkrtz_f16_f32 v19, v89, v91
	ds_write_b128 v5, v[12:15] offset:512
	ds_write_b128 v5, v[16:19] offset:2560
	s_waitcnt vmcnt(0)
	v_cvt_pkrtz_f16_f32 v12, v92, v94
	v_cvt_pkrtz_f16_f32 v13, v96, v98
	v_cvt_pkrtz_f16_f32 v14, v100, v102
	v_cvt_pkrtz_f16_f32 v15, v104, v106
	v_cvt_pkrtz_f16_f32 v16, v93, v95
	v_cvt_pkrtz_f16_f32 v17, v97, v99
	v_cvt_pkrtz_f16_f32 v18, v101, v103
	v_cvt_pkrtz_f16_f32 v19, v105, v107
	ds_write_b128 v5, v[12:15] offset:768
	ds_write_b128 v5, v[16:19] offset:2816
	s_waitcnt lgkmcnt(0)
	s_barrier
	ds_read_b128 v[12:15], v6 offset:0
	ds_read_b128 v[16:19], v6 offset:2048
	ds_read_b128 v[20:23], v7 offset:0
	ds_read_b128 v[24:27], v7 offset:2048
	ds_read_b128 v[28:31], v8 offset:0
	ds_read_b128 v[32:35], v8 offset:2048
	ds_read_b128 v[36:39], v9 offset:0
	ds_read_b128 v[40:43], v9 offset:2048
	s_waitcnt lgkmcnt(7)
	v_mfma_f32_16x16x32_f16 v[188:191], v[116:119], v[12:15], v[188:191]
	v_mfma_f32_16x16x32_f16 v[220:223], v[156:159], v[12:15], v[220:223]
	s_waitcnt lgkmcnt(6)
	v_mfma_f32_16x16x32_f16 v[192:195], v[120:123], v[16:19], v[192:195]
	v_mfma_f32_16x16x32_f16 v[224:227], v[160:163], v[16:19], v[224:227]
	s_waitcnt lgkmcnt(5)
	v_mfma_f32_16x16x32_f16 v[196:199], v[124:127], v[20:23], v[196:199]
	v_mfma_f32_16x16x32_f16 v[228:231], v[164:167], v[20:23], v[228:231]
	s_waitcnt lgkmcnt(4)
	v_mfma_f32_16x16x32_f16 v[200:203], v[128:131], v[24:27], v[200:203]
	v_mfma_f32_16x16x32_f16 v[232:235], v[168:171], v[24:27], v[232:235]
	s_waitcnt lgkmcnt(3)
	v_mfma_f32_16x16x32_f16 v[204:207], v[132:135], v[28:31], v[204:207]
	v_mfma_f32_16x16x32_f16 v[236:239], v[172:175], v[28:31], v[236:239]
	s_waitcnt lgkmcnt(2)
	v_mfma_f32_16x16x32_f16 v[208:211], v[136:139], v[32:35], v[208:211]
	v_mfma_f32_16x16x32_f16 v[240:243], v[176:179], v[32:35], v[240:243]
	s_waitcnt lgkmcnt(1)
	v_mfma_f32_16x16x32_f16 v[212:215], v[140:143], v[36:39], v[212:215]
	v_mfma_f32_16x16x32_f16 v[244:247], v[180:183], v[36:39], v[244:247]
	s_waitcnt lgkmcnt(0)
	v_mfma_f32_16x16x32_f16 v[216:219], v[144:147], v[40:43], v[216:219]
	v_mfma_f32_16x16x32_f16 v[248:251], v[184:187], v[40:43], v[248:251]
	s_nop 7
	s_nop 3
	v_and_b32_e32 v10, 1, v0
	v_cmp_eq_u32_e32 vcc, 1, v10
	s_nop 1
	v_cndmask_b32_e32 v188, v188, v220, vcc
	v_cndmask_b32_e32 v189, v189, v221, vcc
	v_cndmask_b32_e32 v190, v190, v222, vcc
	v_cndmask_b32_e32 v191, v191, v223, vcc
	v_cndmask_b32_e32 v192, v192, v224, vcc
	v_cndmask_b32_e32 v193, v193, v225, vcc
	v_cndmask_b32_e32 v194, v194, v226, vcc
	v_cndmask_b32_e32 v195, v195, v227, vcc
	v_cndmask_b32_e32 v196, v196, v228, vcc
	v_cndmask_b32_e32 v197, v197, v229, vcc
	v_cndmask_b32_e32 v198, v198, v230, vcc
	v_cndmask_b32_e32 v199, v199, v231, vcc
	v_cndmask_b32_e32 v200, v200, v232, vcc
	v_cndmask_b32_e32 v201, v201, v233, vcc
	v_cndmask_b32_e32 v202, v202, v234, vcc
	v_cndmask_b32_e32 v203, v203, v235, vcc
	v_cndmask_b32_e32 v204, v204, v236, vcc
	v_cndmask_b32_e32 v205, v205, v237, vcc
	v_cndmask_b32_e32 v206, v206, v238, vcc
	v_cndmask_b32_e32 v207, v207, v239, vcc
	v_cndmask_b32_e32 v208, v208, v240, vcc
	v_cndmask_b32_e32 v209, v209, v241, vcc
	v_cndmask_b32_e32 v210, v210, v242, vcc
	v_cndmask_b32_e32 v211, v211, v243, vcc
	v_cndmask_b32_e32 v212, v212, v244, vcc
	v_cndmask_b32_e32 v213, v213, v245, vcc
	v_cndmask_b32_e32 v214, v214, v246, vcc
	v_cndmask_b32_e32 v215, v215, v247, vcc
	v_cndmask_b32_e32 v216, v216, v248, vcc
	v_cndmask_b32_e32 v217, v217, v249, vcc
	v_cndmask_b32_e32 v218, v218, v250, vcc
	v_cndmask_b32_e32 v219, v219, v251, vcc
	s_barrier
	v_lshrrev_b32_e32 v10, 4, v2
	v_lshlrev_b32_e32 v10, 6, v10
	v_and_b32_e32 v12, 15, v2
	v_add_u32_e32 v10, v10, v12
	v_mul_u32_u24_e32 v10, 0x108, v10
	v_lshl_add_u32 v10, v1, 5, v10
	ds_write_b32 v10, v188 offset:0
	ds_write_b32 v10, v189 offset:4224
	ds_write_b32 v10, v190 offset:8448
	ds_write_b32 v10, v191 offset:12672
	ds_write_b32 v10, v192 offset:4
	ds_write_b32 v10, v193 offset:4228
	ds_write_b32 v10, v194 offset:8452
	ds_write_b32 v10, v195 offset:12676
	s_waitcnt lgkmcnt(4)
	ds_write_b32 v10, v196 offset:8
	ds_write_b32 v10, v197 offset:4232
	ds_write_b32 v10, v198 offset:8456
	ds_write_b32 v10, v199 offset:12680
	ds_write_b32 v10, v200 offset:12
	ds_write_b32 v10, v201 offset:4236
	ds_write_b32 v10, v202 offset:8460
	ds_write_b32 v10, v203 offset:12684
	s_waitcnt lgkmcnt(4)
	ds_write_b32 v10, v204 offset:16
	ds_write_b32 v10, v205 offset:4240
	ds_write_b32 v10, v206 offset:8464
	ds_write_b32 v10, v207 offset:12688
	ds_write_b32 v10, v208 offset:20
	ds_write_b32 v10, v209 offset:4244
	ds_write_b32 v10, v210 offset:8468
	ds_write_b32 v10, v211 offset:12692
	s_waitcnt lgkmcnt(4)
	ds_write_b32 v10, v212 offset:24
	ds_write_b32 v10, v213 offset:4248
	ds_write_b32 v10, v214 offset:8472
	ds_write_b32 v10, v215 offset:12696
	ds_write_b32 v10, v216 offset:28
	ds_write_b32 v10, v217 offset:4252
	ds_write_b32 v10, v218 offset:8476
	ds_write_b32 v10, v219 offset:12700
	s_waitcnt lgkmcnt(0)
	s_barrier
	v_lshrrev_b32_e32 v12, 5, v0
	v_mul_u32_u24_e32 v12, 0x108, v12
	v_and_b32_e32 v13, 31, v0
	v_lshl_add_u32 v12, v13, 3, v12
	ds_read_b64 v[44:45], v12 offset:0
	ds_read_b64 v[46:47], v12 offset:4224
	ds_read_b64 v[48:49], v12 offset:8448
	ds_read_b64 v[50:51], v12 offset:12672
	ds_read_b64 v[52:53], v12 offset:16896
	ds_read_b64 v[54:55], v12 offset:21120
	ds_read_b64 v[56:57], v12 offset:25344
	ds_read_b64 v[58:59], v12 offset:29568
	s_waitcnt lgkmcnt(7)
	v_add_f32_e32 v44, v252, v44
	v_add_f32_e32 v45, v253, v45
	s_mov_b32 s40, 0x0
	buffer_store_dwordx2 v[44:45], v11, s[32:35], s40 offen nt
	s_waitcnt lgkmcnt(6)
	v_add_f32_e32 v46, v252, v46
	v_add_f32_e32 v47, v253, v47
	s_mov_b32 s41, 0xf0400
	buffer_store_dwordx2 v[46:47], v11, s[32:35], s41 offen nt
	s_waitcnt lgkmcnt(5)
	v_add_f32_e32 v48, v252, v48
	v_add_f32_e32 v49, v253, v49
	s_mov_b32 s42, 0x1e0800
	buffer_store_dwordx2 v[48:49], v11, s[32:35], s42 offen nt
	s_waitcnt lgkmcnt(4)
	v_add_f32_e32 v50, v252, v50
	v_add_f32_e32 v51, v253, v51
	s_mov_b32 s43, 0x2d0c00
	buffer_store_dwordx2 v[50:51], v11, s[32:35], s43 offen nt
	s_waitcnt lgkmcnt(3)
	v_add_f32_e32 v52, v252, v52
	v_add_f32_e32 v53, v253, v53
	s_mov_b32 s44, 0x3c1000
	buffer_store_dwordx2 v[52:53], v11, s[32:35], s44 offen nt
	s_waitcnt lgkmcnt(2)
	v_add_f32_e32 v54, v252, v54
	v_add_f32_e32 v55, v253, v55
	s_mov_b32 s45, 0x4b1400
	buffer_store_dwordx2 v[54:55], v11, s[32:35], s45 offen nt
	s_waitcnt lgkmcnt(1)
	v_add_f32_e32 v56, v252, v56
	v_add_f32_e32 v57, v253, v57
	s_mov_b32 s46, 0x5a1800
	buffer_store_dwordx2 v[56:57], v11, s[32:35], s46 offen nt
	s_waitcnt lgkmcnt(0)
	v_add_f32_e32 v58, v252, v58
	v_add_f32_e32 v59, v253, v59
	s_mov_b32 s47, 0x691c00
	buffer_store_dwordx2 v[58:59], v11, s[32:35], s47 offen nt
	ds_read_b64 v[60:61], v12 offset:33792
	ds_read_b64 v[62:63], v12 offset:38016
	ds_read_b64 v[64:65], v12 offset:42240
	ds_read_b64 v[66:67], v12 offset:46464
	ds_read_b64 v[68:69], v12 offset:50688
	ds_read_b64 v[70:71], v12 offset:54912
	ds_read_b64 v[72:73], v12 offset:59136
	ds_read_b64 v[74:75], v12 offset:63360
	s_waitcnt lgkmcnt(7)
	v_add_f32_e32 v60, v252, v60
	v_add_f32_e32 v61, v253, v61
	s_mov_b32 s40, 0x782000
	buffer_store_dwordx2 v[60:61], v11, s[32:35], s40 offen nt
	s_waitcnt lgkmcnt(6)
	v_add_f32_e32 v62, v252, v62
	v_add_f32_e32 v63, v253, v63
	s_mov_b32 s41, 0x872400
	buffer_store_dwordx2 v[62:63], v11, s[32:35], s41 offen nt
	s_waitcnt lgkmcnt(5)
	v_add_f32_e32 v64, v252, v64
	v_add_f32_e32 v65, v253, v65
	s_mov_b32 s42, 0x962800
	buffer_store_dwordx2 v[64:65], v11, s[32:35], s42 offen nt
	s_waitcnt lgkmcnt(4)
	v_add_f32_e32 v66, v252, v66
	v_add_f32_e32 v67, v253, v67
	s_mov_b32 s43, 0xa52c00
	buffer_store_dwordx2 v[66:67], v11, s[32:35], s43 offen nt
	s_waitcnt lgkmcnt(3)
	v_add_f32_e32 v68, v252, v68
	v_add_f32_e32 v69, v253, v69
	s_mov_b32 s44, 0xb43000
	buffer_store_dwordx2 v[68:69], v11, s[32:35], s44 offen nt
	s_waitcnt lgkmcnt(2)
	v_add_f32_e32 v70, v252, v70
	v_add_f32_e32 v71, v253, v71
	s_mov_b32 s45, 0xc33400
	buffer_store_dwordx2 v[70:71], v11, s[32:35], s45 offen nt
	s_waitcnt lgkmcnt(1)
	v_add_f32_e32 v72, v252, v72
	v_add_f32_e32 v73, v253, v73
	s_mov_b32 s46, 0xd23800
	buffer_store_dwordx2 v[72:73], v11, s[32:35], s46 offen nt
	s_waitcnt lgkmcnt(0)
	v_add_f32_e32 v74, v252, v74
	v_add_f32_e32 v75, v253, v75
	s_mov_b32 s47, 0xe13c00
	buffer_store_dwordx2 v[74:75], v11, s[32:35], s47 offen nt
	s_endpgm
